# qkv epilogue: rotary cos/sin rows prefetched one row group ahead (was load + vmcnt(0) per group)
# baseline (speedup 1.0000x reference)
.LBB0_2124:
	s_or_b64 exec, exec, s[0:1]
	v_readlane_b32 s68, v254, 24
	v_lshl_add_u32 v168, v188, 2, s56
	s_cmp_gt_i32 s28, 7
	v_readlane_b32 s78, v254, 34
	v_readlane_b32 s79, v254, 35
	v_readlane_b32 s80, v254, 36
	v_readlane_b32 s81, v254, 37
	v_ashrrev_i32_e32 v169, 31, v168
	v_lshlrev_b32_e32 v138, 8, v154
	s_cselect_b32 s0, s80, s78
	s_cselect_b32 s1, s81, s79
	v_lshlrev_b64 v[172:173], 2, v[168:169]
	v_and_b32_e32 v202, 0x7ff00, v138
	s_waitcnt lgkmcnt(0)
	s_barrier
	s_mov_b64 s[98:99], 0x1000
	s_mov_b64 s[100:101], 0x5000
	v_lshl_add_u64 v[122:123], s[0:1], 0, v[172:173]
	v_lshl_add_u64 v[138:139], s[8:9], 0, v[202:203]
	v_lshl_add_u64 v[142:143], s[16:17], 0, v[202:203]
	global_load_dwordx4 v[126:129], v[122:123], off
	s_waitcnt lgkmcnt(0)
	global_load_dwordx4 v[122:125], v[122:123], off offset:256
	v_lshl_add_u64 v[138:139], v[138:139], 0, v[172:173]
	v_lshl_add_u64 v[142:143], v[142:143], 0, v[172:173]
	v_lshl_add_u64 v[244:245], v[138:139], 0, s[98:99]
	v_lshl_add_u64 v[250:251], v[142:143], 0, s[98:99]
	global_load_dwordx4 v[138:141], v[138:139], off
	s_cselect_b32 s2, 0x800, 0
	global_load_dwordx4 v[142:145], v[142:143], off
	global_load_dwordx4 v[244:247], v[244:245], off
	global_load_dwordx4 v[250:253], v[250:251], off
	s_lshl_b32 s21, s28, 8
	s_and_b32 s21, s21, 0x700
	s_or_b32 s2, s2, s21
	s_add_i32 s21, 0, 0x20000
	v_add_u32_e32 v157, s21, v146
	ds_read_b128 v[146:149], v157
	v_mov_b64_e32 v[176:177], s[6:7]
	v_cvt_f32_i32_e32 v131, v131
	v_cvt_f32_i32_e32 v130, v130
	s_waitcnt lgkmcnt(0)
	v_mov_b32_e32 v150, v147
	v_mov_b32_e32 v151, v148
	v_mov_b32_e32 v147, v149
	v_pk_add_f32 v[146:147], v[150:151], v[146:147]
	v_cvt_f32_i32_e32 v133, v133
	v_add_f32_e32 v146, v146, v147
	v_fmamk_f32 v146, v146, 0x3c000000, v235
	v_cmp_gt_f32_e32 vcc, s63, v146
	v_mul_f32_e32 v147, 0x4f800000, v146
	v_cvt_f32_i32_e32 v132, v132
	v_cndmask_b32_e32 v146, v146, v147, vcc
	v_sqrt_f32_e32 v147, v146
	v_cvt_f32_i32_e32 v137, v137
	v_cvt_f32_i32_e32 v136, v136
	v_cvt_f32_i32_e32 v135, v135
	v_add_u32_e32 v148, -1, v147
	v_fma_f32 v149, -v148, v147, v146
	v_cmp_ge_f32_e64 s[0:1], 0, v149
	v_add_u32_e32 v149, 1, v147
	v_cvt_f32_i32_e32 v134, v134
	v_cndmask_b32_e64 v148, v147, v148, s[0:1]
	v_fma_f32 v147, -v149, v147, v146
	v_cmp_lt_f32_e64 s[0:1], 0, v147
	s_lshl_b32 s2, s2, 1
	v_mov_b64_e32 v[216:217], v[108:109]
	v_cndmask_b32_e64 v147, v148, v149, s[0:1]
	v_mul_f32_e32 v148, 0x37800000, v147
	v_cndmask_b32_e32 v147, v147, v148, vcc
	v_cmp_class_f32_e32 vcc, v146, v236
	v_mad_i64_i32 v[178:179], s[0:1], v154, s64, v[176:177]
	s_nop 0
	v_cndmask_b32_e32 v146, v147, v146, vcc
	v_div_scale_f32 v147, s[0:1], v146, v146, 1.0
	v_rcp_f32_e32 v148, v147
	v_lshl_add_u64 v[192:193], v[178:179], 0, s[2:3]
	v_lshlrev_b64 v[178:179], 1, v[168:169]
	v_lshl_add_u64 v[192:193], v[192:193], 0, v[178:179]
	v_fma_f32 v149, -v147, v148, 1.0
	v_fmac_f32_e32 v148, v149, v148
	v_div_scale_f32 v149, vcc, 1.0, v146, 1.0
	v_mul_f32_e32 v150, v149, v148
	v_fma_f32 v151, -v147, v150, v149
	v_fmac_f32_e32 v150, v151, v148
	v_fma_f32 v147, -v147, v150, v149
	v_div_fmas_f32 v147, v147, v148, v150
	v_div_fixup_f32 v146, v147, v146, 1.0
	v_mul_f32_e32 v146, v156, v146
	v_pk_mul_f32 v[132:133], v[146:147], v[132:133] op_sel_hi:[0,1]
	v_pk_mul_f32 v[130:131], v[146:147], v[130:131] op_sel_hi:[0,1]
	v_pk_mul_f32 v[134:135], v[146:147], v[134:135] op_sel_hi:[0,1]
	v_pk_mul_f32 v[136:137], v[146:147], v[136:137] op_sel_hi:[0,1]
	v_mov_b64_e32 v[214:215], v[106:107]
	s_cmp_lt_i32 s28, 8
	v_readlane_b32 s69, v254, 25
	v_readlane_b32 s70, v254, 26
	v_readlane_b32 s71, v254, 27
	v_readlane_b32 s72, v254, 28
	v_readlane_b32 s73, v254, 29
	v_readlane_b32 s74, v254, 30
	v_readlane_b32 s75, v254, 31
	v_readlane_b32 s76, v254, 32
	s_waitcnt vmcnt(2)
	v_pk_mul_f32 v[136:137], v[128:129], v[136:137]
	v_pk_mul_f32 v[130:131], v[122:123], v[130:131]
	v_pk_mul_f32 v[132:133], v[124:125], v[132:133]
	v_pk_mul_f32 v[134:135], v[126:127], v[134:135]
	v_readlane_b32 s77, v254, 33
	v_readlane_b32 s82, v254, 38
	v_pk_mul_f32 v[146:147], v[144:145], v[132:133]
	v_pk_mul_f32 v[148:149], v[142:143], v[130:131]
	v_pk_fma_f32 v[146:147], v[140:141], v[136:137], v[146:147] neg_lo:[0,0,1] neg_hi:[0,0,1]
	v_pk_fma_f32 v[148:149], v[138:139], v[134:135], v[148:149] neg_lo:[0,0,1] neg_hi:[0,0,1]
	v_pk_mul_f32 v[136:137], v[144:145], v[136:137]
	v_pk_mul_f32 v[134:135], v[142:143], v[134:135]
	v_pk_fma_f32 v[152:153], v[140:141], v[132:133], v[136:137]
	v_pk_fma_f32 v[150:151], v[138:139], v[130:131], v[134:135]
	v_pk_add_f32 v[136:137], v[146:147], 0 op_sel_hi:[1,0]
	v_pk_add_f32 v[134:135], v[148:149], 0 op_sel_hi:[1,0]
	v_pk_add_f32 v[132:133], v[152:153], 0 op_sel_hi:[1,0]
	v_pk_add_f32 v[130:131], v[150:151], 0 op_sel_hi:[1,0]
	v_readlane_b32 s83, v254, 39
	v_cvt_pk_bf16_f32 v148, v148, v149
	v_cvt_pk_bf16_f32 v149, v146, v147
	v_cvt_pk_bf16_f32 v146, v150, v151
	v_cvt_pk_bf16_f32 v147, v152, v153
	global_store_dwordx2 v[192:193], v[148:149], off
	global_store_dwordx2 v[192:193], v[146:147], off offset:128
	ds_read_b128 v[146:149], v157 offset:16
	s_waitcnt lgkmcnt(0)
	v_mov_b32_e32 v150, v147
	v_mov_b32_e32 v151, v148
	v_mov_b32_e32 v147, v149
	v_pk_add_f32 v[146:147], v[150:151], v[146:147]
	s_nop 0
	v_add_f32_e32 v146, v146, v147
	v_fmamk_f32 v146, v146, 0x3c000000, v235
	v_cmp_gt_f32_e32 vcc, s63, v146
	v_mul_f32_e32 v147, 0x4f800000, v146
	s_nop 0
	v_cndmask_b32_e32 v146, v146, v147, vcc
	v_sqrt_f32_e32 v147, v146
	s_nop 0
	v_add_u32_e32 v148, -1, v147
	v_fma_f32 v149, -v148, v147, v146
	v_cmp_ge_f32_e64 s[0:1], 0, v149
	v_add_u32_e32 v149, 1, v147
	s_nop 0
	v_cndmask_b32_e64 v148, v147, v148, s[0:1]
	v_fma_f32 v147, -v149, v147, v146
	v_cmp_lt_f32_e64 s[0:1], 0, v147
	s_nop 1
	v_cndmask_b32_e64 v147, v148, v149, s[0:1]
	v_mul_f32_e32 v148, 0x37800000, v147
	v_cndmask_b32_e32 v147, v147, v148, vcc
	v_cmp_class_f32_e32 vcc, v146, v236
	s_nop 1
	v_cndmask_b32_e32 v146, v147, v146, vcc
	v_div_scale_f32 v147, s[0:1], v146, v146, 1.0
	v_rcp_f32_e32 v148, v147
	s_nop 0
	v_fma_f32 v149, -v147, v148, 1.0
	v_fmac_f32_e32 v148, v149, v148
	v_div_scale_f32 v149, vcc, 1.0, v146, 1.0
	v_mul_f32_e32 v150, v149, v148
	v_fma_f32 v151, -v147, v150, v149
	v_fmac_f32_e32 v150, v151, v148
	v_fma_f32 v147, -v147, v150, v149
	v_div_fmas_f32 v147, v147, v148, v150
	v_div_fixup_f32 v157, v147, v146, 1.0
	v_mov_b64_e32 v[148:149], v[116:117]
	v_mov_b64_e32 v[152:153], v[120:121]
	v_mov_b64_e32 v[146:147], v[114:115]
	v_mov_b64_e32 v[150:151], v[118:119]
	v_mul_f32_e32 v202, v156, v157
	v_cvt_f32_i32_e32 v153, v153
	v_cvt_f32_i32_e32 v152, v152
	v_cvt_f32_i32_e32 v151, v151
	v_cvt_f32_i32_e32 v150, v150
	v_cvt_f32_i32_e32 v147, v147
	v_cvt_f32_i32_e32 v146, v146
	v_cvt_f32_i32_e32 v149, v149
	v_cvt_f32_i32_e32 v148, v148
	v_pk_mul_f32 v[150:151], v[202:203], v[150:151] op_sel_hi:[0,1]
	v_pk_mul_f32 v[152:153], v[202:203], v[152:153] op_sel_hi:[0,1]
	v_pk_mul_f32 v[146:147], v[202:203], v[146:147] op_sel_hi:[0,1]
	v_pk_mul_f32 v[148:149], v[202:203], v[148:149] op_sel_hi:[0,1]
	v_pk_mul_f32 v[152:153], v[128:129], v[152:153]
	v_pk_mul_f32 v[150:151], v[126:127], v[150:151]
	v_pk_mul_f32 v[146:147], v[122:123], v[146:147]
	v_pk_mul_f32 v[148:149], v[124:125], v[148:149]
	v_pk_mul_f32 v[212:213], v[142:143], v[146:147]
	v_pk_mul_f32 v[210:211], v[144:145], v[148:149]
	v_pk_mul_f32 v[144:145], v[144:145], v[152:153]
	v_pk_mul_f32 v[142:143], v[142:143], v[150:151]
	v_pk_fma_f32 v[212:213], v[138:139], v[150:151], v[212:213] neg_lo:[0,0,1] neg_hi:[0,0,1]
	v_pk_fma_f32 v[210:211], v[140:141], v[152:153], v[210:211] neg_lo:[0,0,1] neg_hi:[0,0,1]
	v_pk_fma_f32 v[146:147], v[138:139], v[146:147], v[142:143]
	v_pk_fma_f32 v[148:149], v[140:141], v[148:149], v[144:145]
	v_pk_add_f32 v[144:145], v[210:211], 0 op_sel_hi:[1,0]
	v_pk_add_f32 v[142:143], v[212:213], 0 op_sel_hi:[1,0]
	v_pk_add_f32 v[140:141], v[148:149], 0 op_sel_hi:[1,0]
	v_pk_add_f32 v[138:139], v[146:147], 0 op_sel_hi:[1,0]
	v_add_u32_e32 v157, 16, v190
	v_cvt_pk_bf16_f32 v150, v212, v213
	v_cvt_pk_bf16_f32 v151, v210, v211
	v_cvt_pk_bf16_f32 v146, v146, v147
	v_add_u32_e32 v167, s19, v157
	v_cvt_pk_bf16_f32 v147, v148, v149
	global_store_dwordx2 v[192:193], v[150:151], off offset:256
	global_store_dwordx2 v[192:193], v[146:147], off offset:384
	v_lshlrev_b32_e32 v146, 8, v167
	v_and_b32_e32 v202, 0x7ff00, v146
	v_lshl_add_u64 v[146:147], s[8:9], 0, v[202:203]
	v_lshl_add_u64 v[150:151], s[16:17], 0, v[202:203]
	v_lshl_add_u64 v[146:147], v[146:147], 0, v[172:173]
	v_lshl_add_u64 v[150:151], v[150:151], 0, v[172:173]
	s_waitcnt vmcnt(4)
	v_mov_b32_e32 v148, v246
	v_mov_b32_e32 v149, v247
	v_lshl_add_u64 v[246:247], v[146:147], 0, s[98:99]
	v_mov_b32_e32 v146, v244
	v_mov_b32_e32 v147, v245
	global_load_dwordx4 v[244:247], v[246:247], off
	v_lshl_add_u32 v157, v157, 5, s21
	v_mov_b32_e32 v152, v252
	v_mov_b32_e32 v153, v253
	v_lshl_add_u64 v[252:253], v[150:151], 0, s[98:99]
	v_mov_b32_e32 v150, v250
	v_mov_b32_e32 v151, v251
	global_load_dwordx4 v[250:253], v[252:253], off
	ds_read_b128 v[210:213], v157
	s_waitcnt lgkmcnt(0)
	v_mov_b32_e32 v192, v211
	v_mov_b32_e32 v193, v212
	v_mov_b32_e32 v211, v213
	v_pk_add_f32 v[192:193], v[192:193], v[210:211]
	v_mov_b64_e32 v[212:213], v[112:113]
	v_add_f32_e32 v169, v192, v193
	v_fmamk_f32 v169, v169, 0x3c000000, v235
	v_cmp_gt_f32_e32 vcc, s63, v169
	v_mul_f32_e32 v171, 0x4f800000, v169
	v_mov_b64_e32 v[210:211], v[110:111]
	v_cndmask_b32_e32 v169, v169, v171, vcc
	v_sqrt_f32_e32 v171, v169
	s_nop 0
	v_cvt_f32_i32_e32 v193, v213
	v_add_u32_e32 v175, -1, v171
	v_fma_f32 v181, -v175, v171, v169
	v_cmp_ge_f32_e64 s[0:1], 0, v181
	v_add_u32_e32 v181, 1, v171
	v_cvt_f32_i32_e32 v192, v212
	v_cndmask_b32_e64 v175, v171, v175, s[0:1]
	v_fma_f32 v171, -v181, v171, v169
	v_cmp_lt_f32_e64 s[0:1], 0, v171
	v_cvt_f32_i32_e32 v213, v215
	v_cvt_f32_i32_e32 v212, v214
	v_cndmask_b32_e64 v171, v175, v181, s[0:1]
	v_mul_f32_e32 v175, 0x37800000, v171
	v_cndmask_b32_e32 v171, v171, v175, vcc
	v_cmp_class_f32_e32 vcc, v169, v236
	v_cvt_f32_i32_e32 v215, v217
	v_cvt_f32_i32_e32 v214, v216
	v_cndmask_b32_e32 v169, v171, v169, vcc
	v_div_scale_f32 v171, s[0:1], v169, v169, 1.0
	v_rcp_f32_e32 v175, v171
	v_cvt_f32_i32_e32 v211, v211
	v_cvt_f32_i32_e32 v210, v210
	v_fma_f32 v181, -v171, v175, 1.0
	v_fmac_f32_e32 v175, v181, v175
	v_div_scale_f32 v181, vcc, 1.0, v169, 1.0
	v_mul_f32_e32 v183, v181, v175
	v_fma_f32 v185, -v171, v183, v181
	v_fmac_f32_e32 v183, v185, v175
	v_fma_f32 v171, -v171, v183, v181
	v_div_fmas_f32 v171, v171, v175, v183
	v_div_fixup_f32 v169, v171, v169, 1.0
	v_mul_f32_e32 v202, v186, v169
	v_pk_mul_f32 v[214:215], v[202:203], v[214:215] op_sel_hi:[0,1]
	v_pk_mul_f32 v[212:213], v[202:203], v[212:213] op_sel_hi:[0,1]
	v_pk_mul_f32 v[210:211], v[202:203], v[210:211] op_sel_hi:[0,1]
	v_pk_mul_f32 v[192:193], v[202:203], v[192:193] op_sel_hi:[0,1]
	v_pk_mul_f32 v[212:213], v[122:123], v[212:213]
	v_pk_mul_f32 v[214:215], v[124:125], v[214:215]
	v_pk_mul_f32 v[192:193], v[128:129], v[192:193]
	v_pk_mul_f32 v[210:211], v[126:127], v[210:211]
	v_pk_mul_f32 v[216:217], v[152:153], v[214:215]
	v_pk_mul_f32 v[240:241], v[150:151], v[212:213]
	v_pk_fma_f32 v[216:217], v[148:149], v[192:193], v[216:217] neg_lo:[0,0,1] neg_hi:[0,0,1]
	v_pk_fma_f32 v[240:241], v[146:147], v[210:211], v[240:241] neg_lo:[0,0,1] neg_hi:[0,0,1]
	v_pk_mul_f32 v[192:193], v[152:153], v[192:193]
	v_pk_mul_f32 v[210:211], v[150:151], v[210:211]
	v_pk_fma_f32 v[192:193], v[148:149], v[214:215], v[192:193]
	v_pk_fma_f32 v[210:211], v[146:147], v[212:213], v[210:211]
	v_mad_i64_i32 v[212:213], s[0:1], v167, s64, v[176:177]
	v_pk_add_f32 v[136:137], v[136:137], v[216:217]
	v_pk_add_f32 v[134:135], v[134:135], v[240:241]
	v_pk_add_f32 v[132:133], v[132:133], v[192:193]
	v_pk_add_f32 v[130:131], v[130:131], v[210:211]
	v_lshl_add_u64 v[212:213], v[212:213], 0, s[2:3]
	v_lshl_add_u64 v[242:243], v[212:213], 0, v[178:179]
	v_cvt_pk_bf16_f32 v212, v240, v241
	v_cvt_pk_bf16_f32 v213, v216, v217
	v_cvt_pk_bf16_f32 v210, v210, v211
	v_cvt_pk_bf16_f32 v211, v192, v193
	global_store_dwordx2 v[242:243], v[212:213], off
	global_store_dwordx2 v[242:243], v[210:211], off offset:128
	ds_read_b128 v[210:213], v157 offset:16
	v_mov_b64_e32 v[216:217], v[104:105]
	v_mov_b64_e32 v[214:215], v[102:103]
	s_waitcnt lgkmcnt(0)
	v_mov_b32_e32 v192, v211
	v_mov_b32_e32 v193, v212
	v_mov_b32_e32 v211, v213
	v_pk_add_f32 v[192:193], v[192:193], v[210:211]
	v_mov_b64_e32 v[212:213], v[100:101]
	v_add_f32_e32 v157, v192, v193
	v_fmamk_f32 v157, v157, 0x3c000000, v235
	v_cmp_gt_f32_e32 vcc, s63, v157
	v_mul_f32_e32 v167, 0x4f800000, v157
	v_mov_b64_e32 v[210:211], v[98:99]
	v_cndmask_b32_e32 v157, v157, v167, vcc
	v_sqrt_f32_e32 v167, v157
	s_nop 0
	v_cvt_f32_i32_e32 v193, v217
	v_add_u32_e32 v169, -1, v167
	v_fma_f32 v171, -v169, v167, v157
	v_cmp_ge_f32_e64 s[0:1], 0, v171
	v_add_u32_e32 v171, 1, v167
	v_cvt_f32_i32_e32 v192, v216
	v_cndmask_b32_e64 v169, v167, v169, s[0:1]
	v_fma_f32 v167, -v171, v167, v157
	v_cmp_lt_f32_e64 s[0:1], 0, v167
	v_cvt_f32_i32_e32 v215, v215
	v_cvt_f32_i32_e32 v214, v214
	v_cndmask_b32_e64 v167, v169, v171, s[0:1]
	v_mul_f32_e32 v169, 0x37800000, v167
	v_cndmask_b32_e32 v167, v167, v169, vcc
	v_cmp_class_f32_e32 vcc, v157, v236
	v_cvt_f32_i32_e32 v211, v211
	v_cvt_f32_i32_e32 v210, v210
	v_cndmask_b32_e32 v157, v167, v157, vcc
	v_div_scale_f32 v167, s[0:1], v157, v157, 1.0
	v_rcp_f32_e32 v169, v167
	v_cvt_f32_i32_e32 v213, v213
	v_cvt_f32_i32_e32 v212, v212
	v_fma_f32 v171, -v167, v169, 1.0
	v_fmac_f32_e32 v169, v171, v169
	v_div_scale_f32 v171, vcc, 1.0, v157, 1.0
	v_mul_f32_e32 v175, v171, v169
	v_fma_f32 v181, -v167, v175, v171
	v_fmac_f32_e32 v175, v181, v169
	v_fma_f32 v167, -v167, v175, v171
	v_div_fmas_f32 v167, v167, v169, v175
	v_div_fixup_f32 v157, v167, v157, 1.0
	v_mul_f32_e32 v186, v186, v157
	v_pk_mul_f32 v[214:215], v[186:187], v[214:215] op_sel_hi:[0,1]
	v_pk_mul_f32 v[192:193], v[186:187], v[192:193] op_sel_hi:[0,1]
	v_pk_mul_f32 v[212:213], v[186:187], v[212:213] op_sel_hi:[0,1]
	v_pk_mul_f32 v[186:187], v[186:187], v[210:211] op_sel_hi:[0,1]
	v_pk_mul_f32 v[192:193], v[128:129], v[192:193]
	v_pk_mul_f32 v[214:215], v[126:127], v[214:215]
	v_pk_mul_f32 v[186:187], v[122:123], v[186:187]
	v_pk_mul_f32 v[210:211], v[124:125], v[212:213]
	v_pk_mul_f32 v[216:217], v[150:151], v[186:187]
	v_pk_mul_f32 v[212:213], v[152:153], v[210:211]
	v_pk_mul_f32 v[152:153], v[152:153], v[192:193]
	v_pk_mul_f32 v[150:151], v[150:151], v[214:215]
	v_pk_fma_f32 v[216:217], v[146:147], v[214:215], v[216:217] neg_lo:[0,0,1] neg_hi:[0,0,1]
	v_pk_fma_f32 v[212:213], v[148:149], v[192:193], v[212:213] neg_lo:[0,0,1] neg_hi:[0,0,1]
	v_pk_fma_f32 v[146:147], v[146:147], v[186:187], v[150:151]
	v_pk_fma_f32 v[148:149], v[148:149], v[210:211], v[152:153]
	v_pk_add_f32 v[144:145], v[144:145], v[212:213]
	v_pk_add_f32 v[142:143], v[142:143], v[216:217]
	v_pk_add_f32 v[140:141], v[140:141], v[148:149]
	v_pk_add_f32 v[138:139], v[138:139], v[146:147]
	v_add_u32_e32 v157, 32, v190
	v_cvt_pk_bf16_f32 v150, v216, v217
	v_cvt_pk_bf16_f32 v151, v212, v213
	v_cvt_pk_bf16_f32 v146, v146, v147
	v_add_u32_e32 v167, s19, v157
	v_cvt_pk_bf16_f32 v147, v148, v149
	global_store_dwordx2 v[242:243], v[150:151], off offset:256
	global_store_dwordx2 v[242:243], v[146:147], off offset:384
	v_lshlrev_b32_e32 v146, 8, v167
	v_and_b32_e32 v202, 0x7ff00, v146
	v_lshl_add_u64 v[146:147], s[8:9], 0, v[202:203]
	v_lshl_add_u64 v[150:151], s[16:17], 0, v[202:203]
	v_lshl_add_u64 v[146:147], v[146:147], 0, v[172:173]
	v_lshl_add_u64 v[150:151], v[150:151], 0, v[172:173]
	s_waitcnt vmcnt(4)
	v_mov_b32_e32 v148, v246
	v_mov_b32_e32 v149, v247
	v_lshl_add_u64 v[246:247], v[146:147], 0, s[98:99]
	v_mov_b32_e32 v146, v244
	v_mov_b32_e32 v147, v245
	global_load_dwordx4 v[244:247], v[246:247], off
	v_lshl_add_u32 v157, v157, 5, s21
	v_mov_b32_e32 v152, v252
	v_mov_b32_e32 v153, v253
	v_lshl_add_u64 v[252:253], v[150:151], 0, s[98:99]
	v_mov_b32_e32 v150, v250
	v_mov_b32_e32 v151, v251
	global_load_dwordx4 v[250:253], v[252:253], off
	ds_read_b128 v[210:213], v157
	v_mov_b64_e32 v[216:217], v[96:97]
	v_mov_b64_e32 v[214:215], v[94:95]
	s_waitcnt lgkmcnt(0)
	v_mov_b32_e32 v186, v211
	v_mov_b32_e32 v187, v212
	v_mov_b32_e32 v211, v213
	v_pk_add_f32 v[186:187], v[186:187], v[210:211]
	v_mov_b64_e32 v[212:213], v[92:93]
	v_add_f32_e32 v169, v186, v187
	v_fmamk_f32 v169, v169, 0x3c000000, v235
	v_cmp_gt_f32_e32 vcc, s63, v169
	v_mul_f32_e32 v171, 0x4f800000, v169
	v_mov_b64_e32 v[210:211], v[90:91]
	v_cndmask_b32_e32 v169, v169, v171, vcc
	v_sqrt_f32_e32 v171, v169
	s_nop 0
	v_cvt_f32_i32_e32 v211, v211
	v_add_u32_e32 v175, -1, v171
	v_fma_f32 v181, -v175, v171, v169
	v_cmp_ge_f32_e64 s[0:1], 0, v181
	v_add_u32_e32 v181, 1, v171
	v_cvt_f32_i32_e32 v210, v210
	v_cndmask_b32_e64 v175, v171, v175, s[0:1]
	v_fma_f32 v171, -v181, v171, v169
	v_cmp_lt_f32_e64 s[0:1], 0, v171
	v_cvt_f32_i32_e32 v213, v213
	v_cvt_f32_i32_e32 v212, v212
	v_cndmask_b32_e64 v171, v175, v181, s[0:1]
	v_mul_f32_e32 v175, 0x37800000, v171
	v_cndmask_b32_e32 v171, v171, v175, vcc
	v_cmp_class_f32_e32 vcc, v169, v236
	v_cvt_f32_i32_e32 v187, v217
	v_cvt_f32_i32_e32 v186, v216
	v_cndmask_b32_e32 v169, v171, v169, vcc
	v_div_scale_f32 v171, s[0:1], v169, v169, 1.0
	v_rcp_f32_e32 v175, v171
	v_cvt_f32_i32_e32 v193, v215
	v_cvt_f32_i32_e32 v192, v214
	v_fma_f32 v181, -v171, v175, 1.0
	v_fmac_f32_e32 v175, v181, v175
	v_div_scale_f32 v181, vcc, 1.0, v169, 1.0
	v_mul_f32_e32 v183, v181, v175
	v_fma_f32 v185, -v171, v183, v181
	v_fmac_f32_e32 v183, v185, v175
	v_fma_f32 v171, -v171, v183, v181
	v_div_fmas_f32 v171, v171, v175, v183
	v_div_fixup_f32 v169, v171, v169, 1.0
	v_mul_f32_e32 v202, v184, v169
	v_pk_mul_f32 v[212:213], v[202:203], v[212:213] op_sel_hi:[0,1]
	v_pk_mul_f32 v[210:211], v[202:203], v[210:211] op_sel_hi:[0,1]
	v_pk_mul_f32 v[192:193], v[202:203], v[192:193] op_sel_hi:[0,1]
	v_pk_mul_f32 v[186:187], v[202:203], v[186:187] op_sel_hi:[0,1]
	v_pk_mul_f32 v[210:211], v[122:123], v[210:211]
	v_pk_mul_f32 v[212:213], v[124:125], v[212:213]
	v_pk_mul_f32 v[186:187], v[128:129], v[186:187]
	v_pk_mul_f32 v[192:193], v[126:127], v[192:193]
	v_pk_mul_f32 v[214:215], v[152:153], v[212:213]
	v_pk_mul_f32 v[216:217], v[150:151], v[210:211]
	v_pk_fma_f32 v[214:215], v[148:149], v[186:187], v[214:215] neg_lo:[0,0,1] neg_hi:[0,0,1]
	v_pk_fma_f32 v[216:217], v[146:147], v[192:193], v[216:217] neg_lo:[0,0,1] neg_hi:[0,0,1]
	v_pk_mul_f32 v[186:187], v[152:153], v[186:187]
	v_pk_mul_f32 v[192:193], v[150:151], v[192:193]
	v_pk_fma_f32 v[186:187], v[148:149], v[212:213], v[186:187]
	v_pk_fma_f32 v[192:193], v[146:147], v[210:211], v[192:193]
	v_mad_i64_i32 v[210:211], s[0:1], v167, s64, v[176:177]
	v_pk_add_f32 v[136:137], v[136:137], v[214:215]
	v_pk_add_f32 v[134:135], v[134:135], v[216:217]
	v_pk_add_f32 v[132:133], v[132:133], v[186:187]
	v_pk_add_f32 v[130:131], v[130:131], v[192:193]
	v_lshl_add_u64 v[210:211], v[210:211], 0, s[2:3]
	v_lshl_add_u64 v[240:241], v[210:211], 0, v[178:179]
	v_cvt_pk_bf16_f32 v210, v216, v217
	v_cvt_pk_bf16_f32 v211, v214, v215
	v_cvt_pk_bf16_f32 v192, v192, v193
	v_cvt_pk_bf16_f32 v193, v186, v187
	global_store_dwordx2 v[240:241], v[210:211], off
	global_store_dwordx2 v[240:241], v[192:193], off offset:128
	ds_read_b128 v[210:213], v157 offset:16
	v_mov_b64_e32 v[216:217], v[84:85]
	v_mov_b64_e32 v[214:215], v[82:83]
	s_waitcnt lgkmcnt(0)
	v_mov_b32_e32 v186, v211
	v_mov_b32_e32 v187, v212
	v_mov_b32_e32 v211, v213
	v_pk_add_f32 v[186:187], v[186:187], v[210:211]
	v_mov_b64_e32 v[212:213], v[88:89]
	v_add_f32_e32 v157, v186, v187
	v_fmamk_f32 v157, v157, 0x3c000000, v235
	v_cmp_gt_f32_e32 vcc, s63, v157
	v_mul_f32_e32 v167, 0x4f800000, v157
	v_mov_b64_e32 v[210:211], v[86:87]
	v_cndmask_b32_e32 v157, v157, v167, vcc
	v_sqrt_f32_e32 v167, v157
	s_nop 0
	v_cvt_f32_i32_e32 v187, v213
	v_add_u32_e32 v169, -1, v167
	v_fma_f32 v171, -v169, v167, v157
	v_cmp_ge_f32_e64 s[0:1], 0, v171
	v_add_u32_e32 v171, 1, v167
	v_cvt_f32_i32_e32 v186, v212
	v_cndmask_b32_e64 v169, v167, v169, s[0:1]
	v_fma_f32 v167, -v171, v167, v157
	v_cmp_lt_f32_e64 s[0:1], 0, v167
	v_cvt_f32_i32_e32 v193, v211
	v_cvt_f32_i32_e32 v192, v210
	v_cndmask_b32_e64 v167, v169, v171, s[0:1]
	v_mul_f32_e32 v169, 0x37800000, v167
	v_cndmask_b32_e32 v167, v167, v169, vcc
	v_cmp_class_f32_e32 vcc, v157, v236
	v_cvt_f32_i32_e32 v211, v215
	v_cvt_f32_i32_e32 v210, v214
	v_cndmask_b32_e32 v157, v167, v157, vcc
	v_div_scale_f32 v167, s[0:1], v157, v157, 1.0
	v_rcp_f32_e32 v169, v167
	v_cvt_f32_i32_e32 v213, v217
	v_cvt_f32_i32_e32 v212, v216
	v_fma_f32 v171, -v167, v169, 1.0
	v_fmac_f32_e32 v169, v171, v169
	v_div_scale_f32 v171, vcc, 1.0, v157, 1.0
	v_mul_f32_e32 v175, v171, v169
	v_fma_f32 v181, -v167, v175, v171
	v_fmac_f32_e32 v175, v181, v169
	v_fma_f32 v167, -v167, v175, v171
	v_div_fmas_f32 v167, v167, v169, v175
	v_div_fixup_f32 v157, v167, v157, 1.0
	v_mul_f32_e32 v184, v184, v157
	v_pk_mul_f32 v[192:193], v[184:185], v[192:193] op_sel_hi:[0,1]
	v_pk_mul_f32 v[186:187], v[184:185], v[186:187] op_sel_hi:[0,1]
	v_pk_mul_f32 v[212:213], v[184:185], v[212:213] op_sel_hi:[0,1]
	v_pk_mul_f32 v[184:185], v[184:185], v[210:211] op_sel_hi:[0,1]
	v_pk_mul_f32 v[186:187], v[128:129], v[186:187]
	v_pk_mul_f32 v[192:193], v[126:127], v[192:193]
	v_pk_mul_f32 v[184:185], v[122:123], v[184:185]
	v_pk_mul_f32 v[210:211], v[124:125], v[212:213]
	v_pk_mul_f32 v[214:215], v[150:151], v[184:185]
	v_pk_mul_f32 v[212:213], v[152:153], v[210:211]
	v_pk_mul_f32 v[152:153], v[152:153], v[186:187]
	v_pk_mul_f32 v[150:151], v[150:151], v[192:193]
	v_pk_fma_f32 v[214:215], v[146:147], v[192:193], v[214:215] neg_lo:[0,0,1] neg_hi:[0,0,1]
	v_pk_fma_f32 v[212:213], v[148:149], v[186:187], v[212:213] neg_lo:[0,0,1] neg_hi:[0,0,1]
	v_pk_fma_f32 v[146:147], v[146:147], v[184:185], v[150:151]
	v_pk_fma_f32 v[148:149], v[148:149], v[210:211], v[152:153]
	v_pk_add_f32 v[144:145], v[144:145], v[212:213]
	v_pk_add_f32 v[142:143], v[142:143], v[214:215]
	v_pk_add_f32 v[140:141], v[140:141], v[148:149]
	v_pk_add_f32 v[138:139], v[138:139], v[146:147]
	v_add_u32_e32 v157, 48, v190
	v_cvt_pk_bf16_f32 v150, v214, v215
	v_cvt_pk_bf16_f32 v151, v212, v213
	v_cvt_pk_bf16_f32 v146, v146, v147
	v_add_u32_e32 v167, s19, v157
	v_cvt_pk_bf16_f32 v147, v148, v149
	global_store_dwordx2 v[240:241], v[150:151], off offset:256
	global_store_dwordx2 v[240:241], v[146:147], off offset:384
	v_lshlrev_b32_e32 v146, 8, v167
	v_and_b32_e32 v202, 0x7ff00, v146
	v_lshl_add_u64 v[146:147], s[8:9], 0, v[202:203]
	v_lshl_add_u64 v[150:151], s[16:17], 0, v[202:203]
	v_lshl_add_u64 v[146:147], v[146:147], 0, v[172:173]
	v_lshl_add_u64 v[150:151], v[150:151], 0, v[172:173]
	s_waitcnt vmcnt(4)
	v_mov_b32_e32 v148, v246
	v_mov_b32_e32 v149, v247
	v_lshl_add_u64 v[246:247], v[146:147], 0, s[100:101]
	v_mov_b32_e32 v146, v244
	v_mov_b32_e32 v147, v245
	global_load_dwordx4 v[244:247], v[246:247], off
	v_lshl_add_u32 v157, v157, 5, s21
	v_mov_b32_e32 v152, v252
	v_mov_b32_e32 v153, v253
	v_lshl_add_u64 v[252:253], v[150:151], 0, s[100:101]
	v_mov_b32_e32 v150, v250
	v_mov_b32_e32 v151, v251
	global_load_dwordx4 v[250:253], v[252:253], off
	ds_read_b128 v[184:187], v157
	v_mov_b64_e32 v[212:213], v[80:81]
	v_mov_b64_e32 v[210:211], v[78:79]
	s_waitcnt lgkmcnt(0)
	v_mov_b32_e32 v192, v185
	v_mov_b32_e32 v193, v186
	v_mov_b32_e32 v185, v187
	v_pk_add_f32 v[184:185], v[192:193], v[184:185]
	s_nop 0
	v_add_f32_e32 v169, v184, v185
	v_fmamk_f32 v169, v169, 0x3c000000, v235
	v_cmp_gt_f32_e32 vcc, s63, v169
	v_mul_f32_e32 v171, 0x4f800000, v169
	s_nop 0
	v_cndmask_b32_e32 v169, v169, v171, vcc
	v_sqrt_f32_e32 v171, v169
	s_nop 0
	v_add_u32_e32 v175, -1, v171
	v_fma_f32 v181, -v175, v171, v169
	v_cmp_ge_f32_e64 s[0:1], 0, v181
	v_add_u32_e32 v181, 1, v171
	s_nop 0
	v_cndmask_b32_e64 v175, v171, v175, s[0:1]
	v_fma_f32 v171, -v181, v171, v169
	v_cmp_lt_f32_e64 s[0:1], 0, v171
	s_nop 1
	v_cndmask_b32_e64 v171, v175, v181, s[0:1]
	v_mul_f32_e32 v175, 0x37800000, v171
	v_cndmask_b32_e32 v171, v171, v175, vcc
	v_cmp_class_f32_e32 vcc, v169, v236
	s_nop 1
	v_cndmask_b32_e32 v169, v171, v169, vcc
	v_div_scale_f32 v171, s[0:1], v169, v169, 1.0
	v_rcp_f32_e32 v175, v171
	s_nop 0
	v_fma_f32 v181, -v171, v175, 1.0
	v_fmac_f32_e32 v175, v181, v175
	v_div_scale_f32 v181, vcc, 1.0, v169, 1.0
	v_mul_f32_e32 v183, v181, v175
	v_fma_f32 v184, -v171, v183, v181
	v_fmac_f32_e32 v183, v184, v175
	v_mov_b64_e32 v[186:187], v[76:77]
	v_mov_b64_e32 v[184:185], v[74:75]
	v_fma_f32 v171, -v171, v183, v181
	v_cvt_f32_i32_e32 v185, v185
	v_cvt_f32_i32_e32 v184, v184
	v_cvt_f32_i32_e32 v187, v187
	v_cvt_f32_i32_e32 v186, v186
	v_div_fmas_f32 v171, v171, v175, v183
	v_cvt_f32_i32_e32 v193, v213
	v_cvt_f32_i32_e32 v192, v212
	v_cvt_f32_i32_e32 v211, v211
	v_cvt_f32_i32_e32 v210, v210
	v_div_fixup_f32 v169, v171, v169, 1.0
	v_mul_f32_e32 v202, v182, v169
	v_pk_mul_f32 v[186:187], v[202:203], v[186:187] op_sel_hi:[0,1]
	v_pk_mul_f32 v[184:185], v[202:203], v[184:185] op_sel_hi:[0,1]
	v_pk_mul_f32 v[210:211], v[202:203], v[210:211] op_sel_hi:[0,1]
	v_pk_mul_f32 v[192:193], v[202:203], v[192:193] op_sel_hi:[0,1]
	v_pk_mul_f32 v[184:185], v[122:123], v[184:185]
	v_pk_mul_f32 v[186:187], v[124:125], v[186:187]
	v_pk_mul_f32 v[192:193], v[128:129], v[192:193]
	v_pk_mul_f32 v[210:211], v[126:127], v[210:211]
	v_pk_mul_f32 v[212:213], v[152:153], v[186:187]
	v_pk_mul_f32 v[214:215], v[150:151], v[184:185]
	v_pk_fma_f32 v[212:213], v[148:149], v[192:193], v[212:213] neg_lo:[0,0,1] neg_hi:[0,0,1]
	v_pk_fma_f32 v[214:215], v[146:147], v[210:211], v[214:215] neg_lo:[0,0,1] neg_hi:[0,0,1]
	v_pk_mul_f32 v[192:193], v[152:153], v[192:193]
	v_pk_mul_f32 v[210:211], v[150:151], v[210:211]
	v_pk_fma_f32 v[186:187], v[148:149], v[186:187], v[192:193]
	v_pk_fma_f32 v[184:185], v[146:147], v[184:185], v[210:211]
	v_mad_i64_i32 v[192:193], s[0:1], v167, s64, v[176:177]
	v_pk_add_f32 v[136:137], v[136:137], v[212:213]
	v_pk_add_f32 v[134:135], v[134:135], v[214:215]
	v_pk_add_f32 v[132:133], v[132:133], v[186:187]
	v_pk_add_f32 v[130:131], v[130:131], v[184:185]
	v_lshl_add_u64 v[192:193], v[192:193], 0, s[2:3]
	v_lshl_add_u64 v[192:193], v[192:193], 0, v[178:179]
	v_cvt_pk_bf16_f32 v210, v214, v215
	v_cvt_pk_bf16_f32 v211, v212, v213
	v_cvt_pk_bf16_f32 v184, v184, v185
	v_cvt_pk_bf16_f32 v185, v186, v187
	global_store_dwordx2 v[192:193], v[210:211], off
	global_store_dwordx2 v[192:193], v[184:185], off offset:128
	ds_read_b128 v[184:187], v157 offset:16
	s_waitcnt lgkmcnt(0)
	v_mov_b32_e32 v210, v185
	v_mov_b32_e32 v211, v186
	v_mov_b32_e32 v185, v187
	v_pk_add_f32 v[184:185], v[210:211], v[184:185]
	v_mov_b64_e32 v[212:213], v[68:69]
	v_add_f32_e32 v157, v184, v185
	v_fmamk_f32 v157, v157, 0x3c000000, v235
	v_cmp_gt_f32_e32 vcc, s63, v157
	v_mul_f32_e32 v167, 0x4f800000, v157
	v_mov_b64_e32 v[186:187], v[72:73]
	v_cndmask_b32_e32 v157, v157, v167, vcc
	v_sqrt_f32_e32 v167, v157
	v_mov_b64_e32 v[184:185], v[70:71]
	v_mov_b64_e32 v[210:211], v[66:67]
	v_add_u32_e32 v169, -1, v167
	v_fma_f32 v171, -v169, v167, v157
	v_cmp_ge_f32_e64 s[0:1], 0, v171
	v_add_u32_e32 v171, 1, v167
	v_cvt_f32_i32_e32 v187, v187
	v_cndmask_b32_e64 v169, v167, v169, s[0:1]
	v_fma_f32 v167, -v171, v167, v157
	v_cmp_lt_f32_e64 s[0:1], 0, v167
	v_cvt_f32_i32_e32 v186, v186
	v_cvt_f32_i32_e32 v185, v185
	v_cndmask_b32_e64 v167, v169, v171, s[0:1]
	v_mul_f32_e32 v169, 0x37800000, v167
	v_cndmask_b32_e32 v167, v167, v169, vcc
	v_cmp_class_f32_e32 vcc, v157, v236
	v_cvt_f32_i32_e32 v184, v184
	v_cvt_f32_i32_e32 v211, v211
	v_cndmask_b32_e32 v157, v167, v157, vcc
	v_div_scale_f32 v167, s[0:1], v157, v157, 1.0
	v_rcp_f32_e32 v169, v167
	v_cvt_f32_i32_e32 v210, v210
	v_cvt_f32_i32_e32 v213, v213
	v_cvt_f32_i32_e32 v212, v212
	v_fma_f32 v171, -v167, v169, 1.0
	v_fmac_f32_e32 v169, v171, v169
	v_div_scale_f32 v171, vcc, 1.0, v157, 1.0
	v_mul_f32_e32 v175, v171, v169
	v_fma_f32 v181, -v167, v175, v171
	v_fmac_f32_e32 v175, v181, v169
	v_fma_f32 v167, -v167, v175, v171
	v_div_fmas_f32 v167, v167, v169, v175
	v_div_fixup_f32 v157, v167, v157, 1.0
	v_mul_f32_e32 v182, v182, v157
	v_pk_mul_f32 v[184:185], v[182:183], v[184:185] op_sel_hi:[0,1]
	v_pk_mul_f32 v[186:187], v[182:183], v[186:187] op_sel_hi:[0,1]
	v_pk_mul_f32 v[212:213], v[182:183], v[212:213] op_sel_hi:[0,1]
	v_pk_mul_f32 v[182:183], v[182:183], v[210:211] op_sel_hi:[0,1]
	v_pk_mul_f32 v[186:187], v[128:129], v[186:187]
	v_pk_mul_f32 v[184:185], v[126:127], v[184:185]
	v_pk_mul_f32 v[182:183], v[122:123], v[182:183]
	v_pk_mul_f32 v[210:211], v[124:125], v[212:213]
	v_pk_mul_f32 v[214:215], v[150:151], v[182:183]
	v_pk_mul_f32 v[212:213], v[152:153], v[210:211]
	v_pk_mul_f32 v[152:153], v[152:153], v[186:187]
	v_pk_mul_f32 v[150:151], v[150:151], v[184:185]
	v_pk_fma_f32 v[214:215], v[146:147], v[184:185], v[214:215] neg_lo:[0,0,1] neg_hi:[0,0,1]
	v_pk_fma_f32 v[212:213], v[148:149], v[186:187], v[212:213] neg_lo:[0,0,1] neg_hi:[0,0,1]
	v_pk_fma_f32 v[146:147], v[146:147], v[182:183], v[150:151]
	v_pk_fma_f32 v[148:149], v[148:149], v[210:211], v[152:153]
	v_pk_add_f32 v[144:145], v[144:145], v[212:213]
	v_pk_add_f32 v[142:143], v[142:143], v[214:215]
	v_pk_add_f32 v[140:141], v[140:141], v[148:149]
	v_pk_add_f32 v[138:139], v[138:139], v[146:147]
	v_add_u32_e32 v157, 0x80, v190
	v_cvt_pk_bf16_f32 v150, v214, v215
	v_cvt_pk_bf16_f32 v151, v212, v213
	v_cvt_pk_bf16_f32 v146, v146, v147
	v_add_u32_e32 v167, s19, v157
	v_cvt_pk_bf16_f32 v147, v148, v149
	global_store_dwordx2 v[192:193], v[150:151], off offset:256
	global_store_dwordx2 v[192:193], v[146:147], off offset:384
	v_lshlrev_b32_e32 v146, 8, v167
	v_and_b32_e32 v202, 0x7ff00, v146
	v_lshl_add_u64 v[146:147], s[8:9], 0, v[202:203]
	v_lshl_add_u64 v[150:151], s[16:17], 0, v[202:203]
	v_lshl_add_u64 v[146:147], v[146:147], 0, v[172:173]
	v_lshl_add_u64 v[150:151], v[150:151], 0, v[172:173]
	s_waitcnt vmcnt(4)
	v_mov_b32_e32 v148, v246
	v_mov_b32_e32 v149, v247
	v_lshl_add_u64 v[246:247], v[146:147], 0, s[98:99]
	v_mov_b32_e32 v146, v244
	v_mov_b32_e32 v147, v245
	global_load_dwordx4 v[244:247], v[246:247], off
	v_lshl_add_u32 v157, v157, 5, s21
	v_mov_b32_e32 v152, v252
	v_mov_b32_e32 v153, v253
	v_lshl_add_u64 v[252:253], v[150:151], 0, s[98:99]
	v_mov_b32_e32 v150, v250
	v_mov_b32_e32 v151, v251
	global_load_dwordx4 v[250:253], v[252:253], off
	ds_read_b128 v[182:185], v157
	v_mov_b64_e32 v[212:213], v[64:65]
	v_mov_b64_e32 v[210:211], v[62:63]
	s_waitcnt lgkmcnt(0)
	v_mov_b32_e32 v186, v183
	v_mov_b32_e32 v187, v184
	v_mov_b32_e32 v183, v185
	v_pk_add_f32 v[182:183], v[186:187], v[182:183]
	s_nop 0
	v_add_f32_e32 v169, v182, v183
	v_fmamk_f32 v169, v169, 0x3c000000, v235
	v_cmp_gt_f32_e32 vcc, s63, v169
	v_mul_f32_e32 v171, 0x4f800000, v169
	s_nop 0
	v_cndmask_b32_e32 v169, v169, v171, vcc
	v_sqrt_f32_e32 v171, v169
	s_nop 0
	v_add_u32_e32 v175, -1, v171
	v_fma_f32 v181, -v175, v171, v169
	v_cmp_ge_f32_e64 s[0:1], 0, v181
	v_add_u32_e32 v181, 1, v171
	s_nop 0
	v_cndmask_b32_e64 v175, v171, v175, s[0:1]
	v_fma_f32 v171, -v181, v171, v169
	v_cmp_lt_f32_e64 s[0:1], 0, v171
	s_nop 1
	v_cndmask_b32_e64 v171, v175, v181, s[0:1]
	v_mul_f32_e32 v175, 0x37800000, v171
	v_cndmask_b32_e32 v171, v171, v175, vcc
	v_cmp_class_f32_e32 vcc, v169, v236
	s_nop 1
	v_cndmask_b32_e32 v169, v171, v169, vcc
	v_div_scale_f32 v171, s[0:1], v169, v169, 1.0
	v_rcp_f32_e32 v175, v171
	s_nop 0
	v_fma_f32 v181, -v171, v175, 1.0
	v_fmac_f32_e32 v175, v181, v175
	v_div_scale_f32 v181, vcc, 1.0, v169, 1.0
	v_mul_f32_e32 v182, v181, v175
	v_fma_f32 v183, -v171, v182, v181
	v_fmac_f32_e32 v182, v183, v175
	v_fma_f32 v171, -v171, v182, v181
	v_div_fmas_f32 v171, v171, v175, v182
	v_mov_b64_e32 v[184:185], v[60:61]
	v_mov_b64_e32 v[182:183], v[58:59]
	v_div_fixup_f32 v169, v171, v169, 1.0
	v_cvt_f32_i32_e32 v183, v183
	v_cvt_f32_i32_e32 v182, v182
	v_cvt_f32_i32_e32 v185, v185
	v_cvt_f32_i32_e32 v184, v184
	v_cvt_f32_i32_e32 v187, v213
	v_cvt_f32_i32_e32 v186, v212
	v_cvt_f32_i32_e32 v193, v211
	v_cvt_f32_i32_e32 v192, v210
	v_mul_f32_e32 v202, v180, v169
	v_pk_mul_f32 v[184:185], v[202:203], v[184:185] op_sel_hi:[0,1]
	v_pk_mul_f32 v[182:183], v[202:203], v[182:183] op_sel_hi:[0,1]
	v_pk_mul_f32 v[192:193], v[202:203], v[192:193] op_sel_hi:[0,1]
	v_pk_mul_f32 v[186:187], v[202:203], v[186:187] op_sel_hi:[0,1]
	v_pk_mul_f32 v[182:183], v[122:123], v[182:183]
	v_pk_mul_f32 v[184:185], v[124:125], v[184:185]
	v_pk_mul_f32 v[186:187], v[128:129], v[186:187]
	v_pk_mul_f32 v[192:193], v[126:127], v[192:193]
	v_pk_mul_f32 v[210:211], v[152:153], v[184:185]
	v_pk_mul_f32 v[212:213], v[150:151], v[182:183]
	v_pk_fma_f32 v[210:211], v[148:149], v[186:187], v[210:211] neg_lo:[0,0,1] neg_hi:[0,0,1]
	v_pk_fma_f32 v[212:213], v[146:147], v[192:193], v[212:213] neg_lo:[0,0,1] neg_hi:[0,0,1]
	v_pk_mul_f32 v[186:187], v[152:153], v[186:187]
	v_pk_mul_f32 v[192:193], v[150:151], v[192:193]
	v_pk_fma_f32 v[184:185], v[148:149], v[184:185], v[186:187]
	v_pk_fma_f32 v[182:183], v[146:147], v[182:183], v[192:193]
	v_mad_i64_i32 v[186:187], s[0:1], v167, s64, v[176:177]
	v_pk_add_f32 v[136:137], v[136:137], v[210:211]
	v_pk_add_f32 v[134:135], v[134:135], v[212:213]
	v_pk_add_f32 v[132:133], v[132:133], v[184:185]
	v_pk_add_f32 v[130:131], v[130:131], v[182:183]
	v_lshl_add_u64 v[186:187], v[186:187], 0, s[2:3]
	v_lshl_add_u64 v[186:187], v[186:187], 0, v[178:179]
	v_cvt_pk_bf16_f32 v192, v212, v213
	v_cvt_pk_bf16_f32 v193, v210, v211
	v_cvt_pk_bf16_f32 v182, v182, v183
	v_cvt_pk_bf16_f32 v183, v184, v185
	global_store_dwordx2 v[186:187], v[192:193], off
	global_store_dwordx2 v[186:187], v[182:183], off offset:128
	ds_read_b128 v[182:185], v157 offset:16
	v_mov_b64_e32 v[212:213], v[52:53]
	v_mov_b64_e32 v[210:211], v[50:51]
	s_waitcnt lgkmcnt(0)
	v_mov_b32_e32 v192, v183
	v_mov_b32_e32 v193, v184
	v_mov_b32_e32 v183, v185
	v_pk_add_f32 v[182:183], v[192:193], v[182:183]
	s_nop 0
	v_add_f32_e32 v157, v182, v183
	v_fmamk_f32 v157, v157, 0x3c000000, v235
	v_cmp_gt_f32_e32 vcc, s63, v157
	v_mul_f32_e32 v167, 0x4f800000, v157
	v_mov_b64_e32 v[184:185], v[56:57]
	v_cndmask_b32_e32 v157, v157, v167, vcc
	v_sqrt_f32_e32 v167, v157
	v_mov_b64_e32 v[182:183], v[54:55]
	v_add_u32_e32 v169, -1, v167
	v_fma_f32 v171, -v169, v167, v157
	v_cmp_ge_f32_e64 s[0:1], 0, v171
	v_add_u32_e32 v171, 1, v167
	v_cvt_f32_i32_e32 v185, v185
	v_cndmask_b32_e64 v169, v167, v169, s[0:1]
	v_fma_f32 v167, -v171, v167, v157
	v_cmp_lt_f32_e64 s[0:1], 0, v167
	v_cvt_f32_i32_e32 v184, v184
	v_cvt_f32_i32_e32 v183, v183
	v_cndmask_b32_e64 v167, v169, v171, s[0:1]
	v_mul_f32_e32 v169, 0x37800000, v167
	v_cndmask_b32_e32 v167, v167, v169, vcc
	v_cmp_class_f32_e32 vcc, v157, v236
	v_cvt_f32_i32_e32 v182, v182
	v_cvt_f32_i32_e32 v193, v211
	v_cndmask_b32_e32 v157, v167, v157, vcc
	v_div_scale_f32 v167, s[0:1], v157, v157, 1.0
	v_rcp_f32_e32 v169, v167
	v_cvt_f32_i32_e32 v192, v210
	v_cvt_f32_i32_e32 v211, v213
	v_cvt_f32_i32_e32 v210, v212
	v_fma_f32 v171, -v167, v169, 1.0
	v_fmac_f32_e32 v169, v171, v169
	v_div_scale_f32 v171, vcc, 1.0, v157, 1.0
	v_mul_f32_e32 v175, v171, v169
	v_fma_f32 v181, -v167, v175, v171
	v_fmac_f32_e32 v175, v181, v169
	v_fma_f32 v167, -v167, v175, v171
	v_div_fmas_f32 v167, v167, v169, v175
	v_div_fixup_f32 v157, v167, v157, 1.0
	v_mul_f32_e32 v180, v180, v157
	v_pk_mul_f32 v[182:183], v[180:181], v[182:183] op_sel_hi:[0,1]
	v_pk_mul_f32 v[184:185], v[180:181], v[184:185] op_sel_hi:[0,1]
	v_pk_mul_f32 v[210:211], v[180:181], v[210:211] op_sel_hi:[0,1]
	v_pk_mul_f32 v[180:181], v[180:181], v[192:193] op_sel_hi:[0,1]
	v_pk_mul_f32 v[184:185], v[128:129], v[184:185]
	v_pk_mul_f32 v[182:183], v[126:127], v[182:183]
	v_pk_mul_f32 v[180:181], v[122:123], v[180:181]
	v_pk_mul_f32 v[192:193], v[124:125], v[210:211]
	v_pk_mul_f32 v[212:213], v[150:151], v[180:181]
	v_pk_mul_f32 v[210:211], v[152:153], v[192:193]
	v_pk_mul_f32 v[152:153], v[152:153], v[184:185]
	v_pk_mul_f32 v[150:151], v[150:151], v[182:183]
	v_pk_fma_f32 v[212:213], v[146:147], v[182:183], v[212:213] neg_lo:[0,0,1] neg_hi:[0,0,1]
	v_pk_fma_f32 v[210:211], v[148:149], v[184:185], v[210:211] neg_lo:[0,0,1] neg_hi:[0,0,1]
	v_pk_fma_f32 v[146:147], v[146:147], v[180:181], v[150:151]
	v_pk_fma_f32 v[148:149], v[148:149], v[192:193], v[152:153]
	v_pk_add_f32 v[144:145], v[144:145], v[210:211]
	v_pk_add_f32 v[142:143], v[142:143], v[212:213]
	v_pk_add_f32 v[140:141], v[140:141], v[148:149]
	v_pk_add_f32 v[138:139], v[138:139], v[146:147]
	v_add_u32_e32 v157, 0x90, v190
	v_cvt_pk_bf16_f32 v150, v212, v213
	v_cvt_pk_bf16_f32 v151, v210, v211
	v_cvt_pk_bf16_f32 v146, v146, v147
	v_add_u32_e32 v167, s19, v157
	v_cvt_pk_bf16_f32 v147, v148, v149
	global_store_dwordx2 v[186:187], v[150:151], off offset:256
	global_store_dwordx2 v[186:187], v[146:147], off offset:384
	v_lshlrev_b32_e32 v146, 8, v167
	v_and_b32_e32 v202, 0x7ff00, v146
	v_lshl_add_u64 v[146:147], s[8:9], 0, v[202:203]
	v_lshl_add_u64 v[150:151], s[16:17], 0, v[202:203]
	v_lshl_add_u64 v[146:147], v[146:147], 0, v[172:173]
	v_lshl_add_u64 v[150:151], v[150:151], 0, v[172:173]
	s_waitcnt vmcnt(4)
	v_mov_b32_e32 v148, v246
	v_mov_b32_e32 v149, v247
	v_lshl_add_u64 v[246:247], v[146:147], 0, s[98:99]
	v_mov_b32_e32 v146, v244
	v_mov_b32_e32 v147, v245
	global_load_dwordx4 v[244:247], v[246:247], off
	v_lshl_add_u32 v157, v157, 5, s21
	v_mov_b32_e32 v152, v252
	v_mov_b32_e32 v153, v253
	v_lshl_add_u64 v[252:253], v[150:151], 0, s[98:99]
	v_mov_b32_e32 v150, v250
	v_mov_b32_e32 v151, v251
	global_load_dwordx4 v[250:253], v[252:253], off
	ds_read_b128 v[180:183], v157
	s_waitcnt lgkmcnt(0)
	v_mov_b32_e32 v184, v181
	v_mov_b32_e32 v185, v182
	v_mov_b32_e32 v181, v183
	v_pk_add_f32 v[180:181], v[184:185], v[180:181]
	v_mov_b64_e32 v[186:187], v[48:49]
	v_add_f32_e32 v169, v180, v181
	v_fmamk_f32 v169, v169, 0x3c000000, v235
	v_cmp_gt_f32_e32 vcc, s63, v169
	v_mul_f32_e32 v171, 0x4f800000, v169
	v_mov_b64_e32 v[184:185], v[46:47]
	v_cndmask_b32_e32 v169, v169, v171, vcc
	v_sqrt_f32_e32 v171, v169
	s_nop 0
	v_add_u32_e32 v175, -1, v171
	v_fma_f32 v180, -v175, v171, v169
	v_cmp_ge_f32_e64 s[0:1], 0, v180
	v_add_u32_e32 v180, 1, v171
	s_nop 0
	v_cndmask_b32_e64 v175, v171, v175, s[0:1]
	v_fma_f32 v171, -v180, v171, v169
	v_cmp_lt_f32_e64 s[0:1], 0, v171
	s_nop 1
	v_cndmask_b32_e64 v171, v175, v180, s[0:1]
	v_mul_f32_e32 v175, 0x37800000, v171
	v_cndmask_b32_e32 v171, v171, v175, vcc
	v_cmp_class_f32_e32 vcc, v169, v236
	s_nop 1
	v_cndmask_b32_e32 v169, v171, v169, vcc
	v_div_scale_f32 v171, s[0:1], v169, v169, 1.0
	v_rcp_f32_e32 v175, v171
	s_nop 0
	v_fma_f32 v180, -v171, v175, 1.0
	v_fmac_f32_e32 v175, v180, v175
	v_div_scale_f32 v180, vcc, 1.0, v169, 1.0
	v_mul_f32_e32 v181, v180, v175
	v_fma_f32 v182, -v171, v181, v180
	v_fmac_f32_e32 v181, v182, v175
	v_fma_f32 v171, -v171, v181, v180
	v_div_fmas_f32 v171, v171, v175, v181
	v_mov_b64_e32 v[182:183], v[44:45]
	v_mov_b64_e32 v[180:181], v[42:43]
	v_div_fixup_f32 v169, v171, v169, 1.0
	v_cvt_f32_i32_e32 v181, v181
	v_cvt_f32_i32_e32 v180, v180
	v_cvt_f32_i32_e32 v183, v183
	v_cvt_f32_i32_e32 v182, v182
	v_cvt_f32_i32_e32 v187, v187
	v_cvt_f32_i32_e32 v186, v186
	v_cvt_f32_i32_e32 v185, v185
	v_cvt_f32_i32_e32 v184, v184
	v_mul_f32_e32 v192, v174, v169
	v_pk_mul_f32 v[182:183], v[192:193], v[182:183] op_sel_hi:[0,1]
	v_pk_mul_f32 v[180:181], v[192:193], v[180:181] op_sel_hi:[0,1]
	v_pk_mul_f32 v[184:185], v[192:193], v[184:185] op_sel_hi:[0,1]
	v_pk_mul_f32 v[186:187], v[192:193], v[186:187] op_sel_hi:[0,1]
	v_pk_mul_f32 v[180:181], v[122:123], v[180:181]
	v_pk_mul_f32 v[182:183], v[124:125], v[182:183]
	v_pk_mul_f32 v[186:187], v[128:129], v[186:187]
	v_pk_mul_f32 v[184:185], v[126:127], v[184:185]
	v_pk_mul_f32 v[192:193], v[152:153], v[182:183]
	v_pk_mul_f32 v[210:211], v[150:151], v[180:181]
	v_pk_fma_f32 v[192:193], v[148:149], v[186:187], v[192:193] neg_lo:[0,0,1] neg_hi:[0,0,1]
	v_pk_fma_f32 v[210:211], v[146:147], v[184:185], v[210:211] neg_lo:[0,0,1] neg_hi:[0,0,1]
	v_pk_mul_f32 v[186:187], v[152:153], v[186:187]
	v_pk_mul_f32 v[184:185], v[150:151], v[184:185]
	v_pk_fma_f32 v[182:183], v[148:149], v[182:183], v[186:187]
	v_pk_fma_f32 v[180:181], v[146:147], v[180:181], v[184:185]
	v_mad_i64_i32 v[184:185], s[0:1], v167, s64, v[176:177]
	v_pk_add_f32 v[136:137], v[136:137], v[192:193]
	v_pk_add_f32 v[134:135], v[134:135], v[210:211]
	v_pk_add_f32 v[132:133], v[132:133], v[182:183]
	v_pk_add_f32 v[130:131], v[130:131], v[180:181]
	v_lshl_add_u64 v[184:185], v[184:185], 0, s[2:3]
	v_lshl_add_u64 v[212:213], v[184:185], 0, v[178:179]
	v_cvt_pk_bf16_f32 v184, v210, v211
	v_cvt_pk_bf16_f32 v185, v192, v193
	v_cvt_pk_bf16_f32 v180, v180, v181
	v_cvt_pk_bf16_f32 v181, v182, v183
	global_store_dwordx2 v[212:213], v[184:185], off
	global_store_dwordx2 v[212:213], v[180:181], off offset:128
	ds_read_b128 v[180:183], v157 offset:16
	s_waitcnt lgkmcnt(0)
	v_mov_b32_e32 v184, v181
	v_mov_b32_e32 v185, v182
	v_mov_b32_e32 v181, v183
	v_pk_add_f32 v[180:181], v[184:185], v[180:181]
	v_mov_b64_e32 v[186:187], v[40:41]
	v_add_f32_e32 v157, v180, v181
	v_fmamk_f32 v157, v157, 0x3c000000, v235
	v_cmp_gt_f32_e32 vcc, s63, v157
	v_mul_f32_e32 v167, 0x4f800000, v157
	v_mov_b64_e32 v[184:185], v[38:39]
	v_cndmask_b32_e32 v157, v157, v167, vcc
	v_sqrt_f32_e32 v167, v157
	s_nop 0
	v_add_u32_e32 v169, -1, v167
	v_fma_f32 v171, -v169, v167, v157
	v_cmp_ge_f32_e64 s[0:1], 0, v171
	v_add_u32_e32 v171, 1, v167
	s_nop 0
	v_cndmask_b32_e64 v169, v167, v169, s[0:1]
	v_fma_f32 v167, -v171, v167, v157
	v_cmp_lt_f32_e64 s[0:1], 0, v167
	s_nop 1
	v_cndmask_b32_e64 v167, v169, v171, s[0:1]
	v_mul_f32_e32 v169, 0x37800000, v167
	v_cndmask_b32_e32 v167, v167, v169, vcc
	v_cmp_class_f32_e32 vcc, v157, v236
	s_nop 1
	v_cndmask_b32_e32 v157, v167, v157, vcc
	v_div_scale_f32 v167, s[0:1], v157, v157, 1.0
	v_rcp_f32_e32 v169, v167
	s_nop 0
	v_fma_f32 v171, -v167, v169, 1.0
	v_fmac_f32_e32 v169, v171, v169
	v_div_scale_f32 v171, vcc, 1.0, v157, 1.0
	v_mul_f32_e32 v175, v171, v169
	v_fma_f32 v180, -v167, v175, v171
	v_fmac_f32_e32 v175, v180, v169
	v_mov_b64_e32 v[182:183], v[36:37]
	v_mov_b64_e32 v[180:181], v[34:35]
	v_fma_f32 v167, -v167, v175, v171
	v_cvt_f32_i32_e32 v187, v187
	v_cvt_f32_i32_e32 v186, v186
	v_cvt_f32_i32_e32 v185, v185
	v_cvt_f32_i32_e32 v184, v184
	v_cvt_f32_i32_e32 v181, v181
	v_cvt_f32_i32_e32 v180, v180
	v_cvt_f32_i32_e32 v183, v183
	v_cvt_f32_i32_e32 v182, v182
	v_div_fmas_f32 v167, v167, v169, v175
	v_div_fixup_f32 v157, v167, v157, 1.0
	v_mul_f32_e32 v174, v174, v157
	v_pk_mul_f32 v[184:185], v[174:175], v[184:185] op_sel_hi:[0,1]
	v_pk_mul_f32 v[186:187], v[174:175], v[186:187] op_sel_hi:[0,1]
	v_pk_mul_f32 v[182:183], v[174:175], v[182:183] op_sel_hi:[0,1]
	v_pk_mul_f32 v[174:175], v[174:175], v[180:181] op_sel_hi:[0,1]
	v_pk_mul_f32 v[186:187], v[128:129], v[186:187]
	v_pk_mul_f32 v[184:185], v[126:127], v[184:185]
	v_pk_mul_f32 v[174:175], v[122:123], v[174:175]
	v_pk_mul_f32 v[180:181], v[124:125], v[182:183]
	v_pk_mul_f32 v[192:193], v[150:151], v[174:175]
	v_pk_mul_f32 v[182:183], v[152:153], v[180:181]
	v_pk_mul_f32 v[152:153], v[152:153], v[186:187]
	v_pk_mul_f32 v[150:151], v[150:151], v[184:185]
	v_pk_fma_f32 v[192:193], v[146:147], v[184:185], v[192:193] neg_lo:[0,0,1] neg_hi:[0,0,1]
	v_pk_fma_f32 v[182:183], v[148:149], v[186:187], v[182:183] neg_lo:[0,0,1] neg_hi:[0,0,1]
	v_pk_fma_f32 v[150:151], v[146:147], v[174:175], v[150:151]
	v_pk_fma_f32 v[152:153], v[148:149], v[180:181], v[152:153]
	v_pk_add_f32 v[144:145], v[144:145], v[182:183]
	v_pk_add_f32 v[142:143], v[142:143], v[192:193]
	v_pk_add_f32 v[148:149], v[140:141], v[152:153]
	v_pk_add_f32 v[146:147], v[138:139], v[150:151]
	v_add_u32_e32 v157, 0xa0, v190
	v_cvt_pk_bf16_f32 v138, v192, v193
	v_cvt_pk_bf16_f32 v139, v182, v183
	v_add_u32_e32 v167, s19, v157
	v_cvt_pk_bf16_f32 v140, v150, v151
	v_cvt_pk_bf16_f32 v141, v152, v153
	global_store_dwordx2 v[212:213], v[138:139], off offset:256
	global_store_dwordx2 v[212:213], v[140:141], off offset:384
	v_lshlrev_b32_e32 v138, 8, v167
	v_and_b32_e32 v202, 0x7ff00, v138
	v_lshl_add_u64 v[138:139], s[8:9], 0, v[202:203]
	v_lshl_add_u64 v[150:151], s[16:17], 0, v[202:203]
	v_lshl_add_u64 v[138:139], v[138:139], 0, v[172:173]
	v_lshl_add_u64 v[150:151], v[150:151], 0, v[172:173]
	s_waitcnt vmcnt(4)
	v_mov_b32_e32 v140, v246
	v_mov_b32_e32 v141, v247
	v_lshl_add_u64 v[246:247], v[138:139], 0, s[98:99]
	v_mov_b32_e32 v138, v244
	v_mov_b32_e32 v139, v245
	global_load_dwordx4 v[244:247], v[246:247], off
	v_lshl_add_u32 v157, v157, 5, s21
	v_mov_b32_e32 v152, v252
	v_mov_b32_e32 v153, v253
	v_lshl_add_u64 v[252:253], v[150:151], 0, s[98:99]
	v_mov_b32_e32 v150, v250
	v_mov_b32_e32 v151, v251
	global_load_dwordx4 v[250:253], v[252:253], off
	ds_read_b128 v[180:183], v157
	v_mov_b64_e32 v[186:187], v[28:29]
	v_mov_b64_e32 v[184:185], v[26:27]
	s_waitcnt lgkmcnt(0)
	v_mov_b32_e32 v174, v181
	v_mov_b32_e32 v175, v182
	v_mov_b32_e32 v181, v183
	v_pk_add_f32 v[174:175], v[174:175], v[180:181]
	s_nop 0
	v_add_f32_e32 v169, v174, v175
	v_fmamk_f32 v169, v169, 0x3c000000, v235
	v_cmp_gt_f32_e32 vcc, s63, v169
	v_mul_f32_e32 v171, 0x4f800000, v169
	s_nop 0
	v_cndmask_b32_e32 v169, v169, v171, vcc
	v_sqrt_f32_e32 v171, v169
	s_nop 0
	v_add_u32_e32 v174, -1, v171
	v_fma_f32 v175, -v174, v171, v169
	v_cmp_ge_f32_e64 s[0:1], 0, v175
	v_add_u32_e32 v175, 1, v171
	s_nop 0
	v_cndmask_b32_e64 v174, v171, v174, s[0:1]
	v_fma_f32 v171, -v175, v171, v169
	v_cmp_lt_f32_e64 s[0:1], 0, v171
	s_nop 1
	v_cndmask_b32_e64 v171, v174, v175, s[0:1]
	v_mul_f32_e32 v174, 0x37800000, v171
	v_cndmask_b32_e32 v171, v171, v174, vcc
	v_cmp_class_f32_e32 vcc, v169, v236
	s_nop 1
	v_cndmask_b32_e32 v169, v171, v169, vcc
	v_div_scale_f32 v171, s[0:1], v169, v169, 1.0
	v_rcp_f32_e32 v174, v171
	s_nop 0
	v_fma_f32 v175, -v171, v174, 1.0
	v_fmac_f32_e32 v174, v175, v174
	v_div_scale_f32 v175, vcc, 1.0, v169, 1.0
	v_mul_f32_e32 v180, v175, v174
	v_fma_f32 v181, -v171, v180, v175
	v_fmac_f32_e32 v180, v181, v174
	v_fma_f32 v171, -v171, v180, v175
	v_div_fmas_f32 v171, v171, v174, v180
	v_mov_b64_e32 v[182:183], v[32:33]
	v_mov_b64_e32 v[180:181], v[30:31]
	v_div_fixup_f32 v169, v171, v169, 1.0
	v_cvt_f32_i32_e32 v175, v183
	v_cvt_f32_i32_e32 v174, v182
	v_cvt_f32_i32_e32 v181, v181
	v_cvt_f32_i32_e32 v180, v180
	v_cvt_f32_i32_e32 v185, v185
	v_cvt_f32_i32_e32 v184, v184
	v_cvt_f32_i32_e32 v187, v187
	v_cvt_f32_i32_e32 v186, v186
	v_mul_f32_e32 v182, v170, v169
	v_pk_mul_f32 v[180:181], v[182:183], v[180:181] op_sel_hi:[0,1]
	v_pk_mul_f32 v[174:175], v[182:183], v[174:175] op_sel_hi:[0,1]
	v_pk_mul_f32 v[186:187], v[182:183], v[186:187] op_sel_hi:[0,1]
	v_pk_mul_f32 v[182:183], v[182:183], v[184:185] op_sel_hi:[0,1]
	v_pk_mul_f32 v[182:183], v[122:123], v[182:183]
	v_pk_mul_f32 v[184:185], v[124:125], v[186:187]
	v_pk_mul_f32 v[174:175], v[128:129], v[174:175]
	v_pk_mul_f32 v[180:181], v[126:127], v[180:181]
	v_pk_mul_f32 v[186:187], v[152:153], v[184:185]
	v_pk_mul_f32 v[192:193], v[150:151], v[182:183]
	v_pk_fma_f32 v[186:187], v[140:141], v[174:175], v[186:187] neg_lo:[0,0,1] neg_hi:[0,0,1]
	v_pk_fma_f32 v[192:193], v[138:139], v[180:181], v[192:193] neg_lo:[0,0,1] neg_hi:[0,0,1]
	v_pk_mul_f32 v[174:175], v[152:153], v[174:175]
	v_pk_mul_f32 v[180:181], v[150:151], v[180:181]
	v_pk_fma_f32 v[174:175], v[140:141], v[184:185], v[174:175]
	v_pk_fma_f32 v[180:181], v[138:139], v[182:183], v[180:181]
	v_mad_i64_i32 v[182:183], s[0:1], v167, s64, v[176:177]
	v_pk_add_f32 v[136:137], v[136:137], v[186:187]
	v_pk_add_f32 v[134:135], v[134:135], v[192:193]
	v_pk_add_f32 v[132:133], v[132:133], v[174:175]
	v_pk_add_f32 v[130:131], v[130:131], v[180:181]
	v_lshl_add_u64 v[182:183], v[182:183], 0, s[2:3]
	v_lshl_add_u64 v[210:211], v[182:183], 0, v[178:179]
	v_cvt_pk_bf16_f32 v182, v192, v193
	v_cvt_pk_bf16_f32 v183, v186, v187
	v_cvt_pk_bf16_f32 v180, v180, v181
	v_cvt_pk_bf16_f32 v181, v174, v175
	global_store_dwordx2 v[210:211], v[182:183], off
	global_store_dwordx2 v[210:211], v[180:181], off offset:128
	ds_read_b128 v[180:183], v157 offset:16
	v_mov_b64_e32 v[186:187], v[24:25]
	v_mov_b64_e32 v[184:185], v[22:23]
	s_waitcnt lgkmcnt(0)
	v_mov_b32_e32 v174, v181
	v_mov_b32_e32 v175, v182
	v_mov_b32_e32 v181, v183
	v_pk_add_f32 v[174:175], v[174:175], v[180:181]
	v_mov_b64_e32 v[182:183], v[20:21]
	v_add_f32_e32 v157, v174, v175
	v_fmamk_f32 v157, v157, 0x3c000000, v235
	v_cmp_gt_f32_e32 vcc, s63, v157
	v_mul_f32_e32 v167, 0x4f800000, v157
	v_mov_b64_e32 v[180:181], v[18:19]
	v_cndmask_b32_e32 v157, v157, v167, vcc
	v_sqrt_f32_e32 v167, v157
	s_nop 0
	v_cvt_f32_i32_e32 v185, v185
	v_add_u32_e32 v169, -1, v167
	v_fma_f32 v171, -v169, v167, v157
	v_cmp_ge_f32_e64 s[0:1], 0, v171
	v_add_u32_e32 v171, 1, v167
	v_cvt_f32_i32_e32 v184, v184
	v_cndmask_b32_e64 v169, v167, v169, s[0:1]
	v_fma_f32 v167, -v171, v167, v157
	v_cmp_lt_f32_e64 s[0:1], 0, v167
	v_cvt_f32_i32_e32 v181, v181
	v_cvt_f32_i32_e32 v180, v180
	v_cndmask_b32_e64 v167, v169, v171, s[0:1]
	v_mul_f32_e32 v169, 0x37800000, v167
	v_cndmask_b32_e32 v167, v167, v169, vcc
	v_cmp_class_f32_e32 vcc, v157, v236
	v_cvt_f32_i32_e32 v183, v183
	v_cvt_f32_i32_e32 v182, v182
	v_cndmask_b32_e32 v157, v167, v157, vcc
	v_div_scale_f32 v167, s[0:1], v157, v157, 1.0
	v_rcp_f32_e32 v169, v167
	s_nop 0
	v_fma_f32 v171, -v167, v169, 1.0
	v_fmac_f32_e32 v169, v171, v169
	v_div_scale_f32 v171, vcc, 1.0, v157, 1.0
	v_mul_f32_e32 v174, v171, v169
	v_fma_f32 v175, -v167, v174, v171
	v_fmac_f32_e32 v174, v175, v169
	v_fma_f32 v167, -v167, v174, v171
	v_div_fmas_f32 v167, v167, v169, v174
	v_cvt_f32_i32_e32 v175, v187
	v_cvt_f32_i32_e32 v174, v186
	v_div_fixup_f32 v157, v167, v157, 1.0
	v_mul_f32_e32 v170, v170, v157
	v_pk_mul_f32 v[184:185], v[170:171], v[184:185] op_sel_hi:[0,1]
	v_pk_mul_f32 v[174:175], v[170:171], v[174:175] op_sel_hi:[0,1]
	v_pk_mul_f32 v[182:183], v[170:171], v[182:183] op_sel_hi:[0,1]
	v_pk_mul_f32 v[170:171], v[170:171], v[180:181] op_sel_hi:[0,1]
	v_pk_mul_f32 v[174:175], v[128:129], v[174:175]
	v_pk_mul_f32 v[184:185], v[126:127], v[184:185]
	v_pk_mul_f32 v[170:171], v[122:123], v[170:171]
	v_pk_mul_f32 v[180:181], v[124:125], v[182:183]
	v_pk_mul_f32 v[186:187], v[150:151], v[170:171]
	v_pk_mul_f32 v[182:183], v[152:153], v[180:181]
	v_pk_mul_f32 v[152:153], v[152:153], v[174:175]
	v_pk_mul_f32 v[150:151], v[150:151], v[184:185]
	v_pk_fma_f32 v[186:187], v[138:139], v[184:185], v[186:187] neg_lo:[0,0,1] neg_hi:[0,0,1]
	v_pk_fma_f32 v[182:183], v[140:141], v[174:175], v[182:183] neg_lo:[0,0,1] neg_hi:[0,0,1]
	v_pk_fma_f32 v[150:151], v[138:139], v[170:171], v[150:151]
	v_pk_fma_f32 v[152:153], v[140:141], v[180:181], v[152:153]
	v_pk_add_f32 v[140:141], v[144:145], v[182:183]
	v_pk_add_f32 v[138:139], v[142:143], v[186:187]
	v_pk_add_f32 v[144:145], v[148:149], v[152:153]
	v_pk_add_f32 v[142:143], v[146:147], v[150:151]
	v_add_u32_e32 v157, 0xb0, v190
	v_cvt_pk_bf16_f32 v146, v186, v187
	v_cvt_pk_bf16_f32 v147, v182, v183
	v_add_u32_e32 v167, s19, v157
	v_cvt_pk_bf16_f32 v148, v150, v151
	v_cvt_pk_bf16_f32 v149, v152, v153
	global_store_dwordx2 v[210:211], v[146:147], off offset:256
	global_store_dwordx2 v[210:211], v[148:149], off offset:384
	v_lshlrev_b32_e32 v146, 8, v167
	v_and_b32_e32 v202, 0x7ff00, v146
	v_lshl_add_u64 v[146:147], s[8:9], 0, v[202:203]
	v_lshl_add_u64 v[150:151], s[16:17], 0, v[202:203]
	v_lshl_add_u64 v[146:147], v[146:147], 0, v[172:173]
	v_lshl_add_u64 v[150:151], v[150:151], 0, v[172:173]
	s_waitcnt vmcnt(4)
	v_mov_b32_e32 v146, v244
	v_mov_b32_e32 v147, v245
	v_mov_b32_e32 v148, v246
	v_mov_b32_e32 v149, v247
	v_lshl_add_u32 v157, v157, 5, s21
	v_mov_b32_e32 v150, v250
	v_mov_b32_e32 v151, v251
	v_mov_b32_e32 v152, v252
	v_mov_b32_e32 v153, v253
	ds_read_b128 v[170:173], v157
	v_mov_b64_e32 v[182:183], v[12:13]
	v_mov_b64_e32 v[180:181], v[10:11]
	s_waitcnt lgkmcnt(0)
	v_mov_b32_e32 v174, v171
	v_mov_b32_e32 v175, v172
	v_mov_b32_e32 v171, v173
	v_pk_add_f32 v[170:171], v[174:175], v[170:171]
	s_nop 0
	v_add_f32_e32 v169, v170, v171
	v_fmamk_f32 v169, v169, 0x3c000000, v235
	v_cmp_gt_f32_e32 vcc, s63, v169
	v_mul_f32_e32 v170, 0x4f800000, v169
	s_nop 0
	v_cndmask_b32_e32 v169, v169, v170, vcc
	v_sqrt_f32_e32 v170, v169
	s_nop 0
	v_add_u32_e32 v171, -1, v170
	v_fma_f32 v172, -v171, v170, v169
	v_cmp_ge_f32_e64 s[0:1], 0, v172
	v_add_u32_e32 v172, 1, v170
	s_nop 0
	v_cndmask_b32_e64 v171, v170, v171, s[0:1]
	v_fma_f32 v170, -v172, v170, v169
	v_cmp_lt_f32_e64 s[0:1], 0, v170
	s_nop 1
	v_cndmask_b32_e64 v170, v171, v172, s[0:1]
	v_mul_f32_e32 v171, 0x37800000, v170
	v_cndmask_b32_e32 v170, v170, v171, vcc
	v_cmp_class_f32_e32 vcc, v169, v236
	s_nop 1
	v_cndmask_b32_e32 v169, v170, v169, vcc
	v_div_scale_f32 v170, s[0:1], v169, v169, 1.0
	v_rcp_f32_e32 v171, v170
	s_nop 0
	v_fma_f32 v172, -v170, v171, 1.0
	v_fmac_f32_e32 v171, v172, v171
	v_div_scale_f32 v172, vcc, 1.0, v169, 1.0
	v_mul_f32_e32 v173, v172, v171
	v_fma_f32 v174, -v170, v173, v172
	v_fmac_f32_e32 v173, v174, v171
	v_fma_f32 v170, -v170, v173, v172
	v_div_fmas_f32 v170, v170, v171, v173
	v_div_fixup_f32 v169, v170, v169, 1.0
	v_mov_b64_e32 v[172:173], v[16:17]
	v_mov_b64_e32 v[170:171], v[14:15]
	v_mul_f32_e32 v174, v166, v169
	v_cvt_f32_i32_e32 v173, v173
	v_cvt_f32_i32_e32 v172, v172
	v_cvt_f32_i32_e32 v171, v171
	v_cvt_f32_i32_e32 v170, v170
	v_cvt_f32_i32_e32 v181, v181
	v_cvt_f32_i32_e32 v180, v180
	v_cvt_f32_i32_e32 v183, v183
	v_cvt_f32_i32_e32 v182, v182
	v_pk_mul_f32 v[170:171], v[174:175], v[170:171] op_sel_hi:[0,1]
	v_pk_mul_f32 v[172:173], v[174:175], v[172:173] op_sel_hi:[0,1]
	v_pk_mul_f32 v[172:173], v[128:129], v[172:173]
	v_pk_mul_f32 v[182:183], v[174:175], v[182:183] op_sel_hi:[0,1]
	v_pk_mul_f32 v[174:175], v[174:175], v[180:181] op_sel_hi:[0,1]
	v_pk_mul_f32 v[174:175], v[122:123], v[174:175]
	v_pk_mul_f32 v[180:181], v[124:125], v[182:183]
	v_pk_mul_f32 v[170:171], v[126:127], v[170:171]
	v_pk_mul_f32 v[182:183], v[152:153], v[180:181]
	v_pk_mul_f32 v[184:185], v[150:151], v[174:175]
	v_pk_fma_f32 v[182:183], v[148:149], v[172:173], v[182:183] neg_lo:[0,0,1] neg_hi:[0,0,1]
	v_pk_fma_f32 v[184:185], v[146:147], v[170:171], v[184:185] neg_lo:[0,0,1] neg_hi:[0,0,1]
	v_pk_mul_f32 v[172:173], v[152:153], v[172:173]
	v_pk_mul_f32 v[170:171], v[150:151], v[170:171]
	v_pk_fma_f32 v[172:173], v[148:149], v[180:181], v[172:173]
	v_pk_fma_f32 v[170:171], v[146:147], v[174:175], v[170:171]
	v_mad_i64_i32 v[174:175], s[0:1], v167, s64, v[176:177]
	v_pk_add_f32 v[136:137], v[136:137], v[182:183]
	v_pk_add_f32 v[134:135], v[134:135], v[184:185]
	v_pk_add_f32 v[132:133], v[132:133], v[172:173]
	v_pk_add_f32 v[130:131], v[130:131], v[170:171]
	v_lshl_add_u64 v[174:175], v[174:175], 0, s[2:3]
	v_lshl_add_u64 v[178:179], v[174:175], 0, v[178:179]
	v_cvt_pk_bf16_f32 v174, v184, v185
	v_cvt_pk_bf16_f32 v175, v182, v183
	v_cvt_pk_bf16_f32 v170, v170, v171
	v_cvt_pk_bf16_f32 v171, v172, v173
	global_store_dwordx2 v[178:179], v[174:175], off
	global_store_dwordx2 v[178:179], v[170:171], off offset:128
	ds_read_b128 v[170:173], v157 offset:16
	s_waitcnt lgkmcnt(0)
	v_mov_b32_e32 v174, v171
	v_mov_b32_e32 v175, v172
	v_mov_b32_e32 v171, v173
	v_pk_add_f32 v[170:171], v[174:175], v[170:171]
	v_mov_b64_e32 v[176:177], v[8:9]
	v_add_f32_e32 v157, v170, v171
	v_fmamk_f32 v157, v157, 0x3c000000, v235
	v_cmp_gt_f32_e32 vcc, s63, v157
	v_mul_f32_e32 v167, 0x4f800000, v157
	v_mov_b64_e32 v[174:175], v[6:7]
	v_cndmask_b32_e32 v157, v157, v167, vcc
	v_sqrt_f32_e32 v167, v157
	s_nop 0
	v_add_u32_e32 v169, -1, v167
	v_fma_f32 v170, -v169, v167, v157
	v_cmp_ge_f32_e64 s[0:1], 0, v170
	v_add_u32_e32 v170, 1, v167
	s_nop 0
	v_cndmask_b32_e64 v169, v167, v169, s[0:1]
	v_fma_f32 v167, -v170, v167, v157
	v_cmp_lt_f32_e64 s[0:1], 0, v167
	s_nop 1
	v_cndmask_b32_e64 v167, v169, v170, s[0:1]
	v_mul_f32_e32 v169, 0x37800000, v167
	v_cndmask_b32_e32 v167, v167, v169, vcc
	v_cmp_class_f32_e32 vcc, v157, v236
	s_nop 1
	v_cndmask_b32_e32 v157, v167, v157, vcc
	v_div_scale_f32 v167, s[0:1], v157, v157, 1.0
	v_rcp_f32_e32 v169, v167
	s_nop 0
	v_fma_f32 v170, -v167, v169, 1.0
	v_fmac_f32_e32 v169, v170, v169
	v_div_scale_f32 v170, vcc, 1.0, v157, 1.0
	v_mul_f32_e32 v171, v170, v169
	v_fma_f32 v172, -v167, v171, v170
	v_fmac_f32_e32 v171, v172, v169
	v_fma_f32 v167, -v167, v171, v170
	v_div_fmas_f32 v167, v167, v169, v171
	v_mov_b64_e32 v[172:173], v[4:5]
	v_mov_b64_e32 v[170:171], v[2:3]
	v_div_fixup_f32 v157, v167, v157, 1.0
	v_cvt_f32_i32_e32 v177, v177
	v_cvt_f32_i32_e32 v176, v176
	v_cvt_f32_i32_e32 v175, v175
	v_cvt_f32_i32_e32 v174, v174
	v_cvt_f32_i32_e32 v171, v171
	v_cvt_f32_i32_e32 v170, v170
	v_cvt_f32_i32_e32 v173, v173
	v_cvt_f32_i32_e32 v172, v172
	v_mul_f32_e32 v166, v166, v157
	v_pk_mul_f32 v[174:175], v[166:167], v[174:175] op_sel_hi:[0,1]
	v_pk_mul_f32 v[176:177], v[166:167], v[176:177] op_sel_hi:[0,1]
	v_pk_mul_f32 v[172:173], v[166:167], v[172:173] op_sel_hi:[0,1]
	v_pk_mul_f32 v[166:167], v[166:167], v[170:171] op_sel_hi:[0,1]
	v_pk_mul_f32 v[122:123], v[122:123], v[166:167]
	v_pk_mul_f32 v[124:125], v[124:125], v[172:173]
	v_pk_mul_f32 v[128:129], v[128:129], v[176:177]
	v_pk_mul_f32 v[126:127], v[126:127], v[174:175]
	v_pk_mul_f32 v[166:167], v[152:153], v[124:125]
	v_pk_mul_f32 v[170:171], v[150:151], v[122:123]
	v_pk_fma_f32 v[166:167], v[148:149], v[128:129], v[166:167] neg_lo:[0,0,1] neg_hi:[0,0,1]
	v_pk_fma_f32 v[170:171], v[146:147], v[126:127], v[170:171] neg_lo:[0,0,1] neg_hi:[0,0,1]
	v_pk_mul_f32 v[128:129], v[152:153], v[128:129]
	v_pk_mul_f32 v[126:127], v[150:151], v[126:127]
	v_pk_fma_f32 v[148:149], v[148:149], v[124:125], v[128:129]
	v_pk_fma_f32 v[146:147], v[146:147], v[122:123], v[126:127]
	v_pk_add_f32 v[128:129], v[140:141], v[166:167]
	v_pk_add_f32 v[126:127], v[138:139], v[170:171]
	v_pk_add_f32 v[124:125], v[144:145], v[148:149]
	v_pk_add_f32 v[122:123], v[142:143], v[146:147]
	s_nop 0
	v_cvt_pk_bf16_f32 v138, v170, v171
	v_cvt_pk_bf16_f32 v139, v166, v167
	v_cvt_pk_bf16_f32 v140, v146, v147
	v_cvt_pk_bf16_f32 v141, v148, v149
	global_store_dwordx2 v[178:179], v[138:139], off offset:256
	global_store_dwordx2 v[178:179], v[140:141], off offset:384
	s_cbranch_scc1 .LBB0_2160
	v_xor_b32_e32 v138, 1, v238
	v_cmp_lt_i32_e32 vcc, v138, v155
	v_xor_b32_e32 v139, 2, v238
	s_nop 0
	v_cndmask_b32_e32 v138, v238, v138, vcc
	v_lshlrev_b32_e32 v138, 2, v138
	ds_bpermute_b32 v143, v138, v134
	v_cmp_lt_i32_e32 vcc, v139, v155
	s_waitcnt lgkmcnt(0)
	v_add_f32_e32 v134, v134, v143
	v_cndmask_b32_e32 v139, v238, v139, vcc
	v_lshlrev_b32_e32 v140, 2, v139
	ds_bpermute_b32 v143, v140, v134
	v_xor_b32_e32 v139, 4, v238
	v_cmp_lt_i32_e32 vcc, v139, v155
	s_waitcnt lgkmcnt(0)
	v_add_f32_e32 v134, v134, v143
	v_cndmask_b32_e32 v139, v238, v139, vcc
	v_lshlrev_b32_e32 v141, 2, v139
	ds_bpermute_b32 v143, v141, v134
	v_xor_b32_e32 v139, 8, v238
	v_cmp_lt_i32_e32 vcc, v139, v155
	s_waitcnt lgkmcnt(0)
	v_add_f32_e32 v134, v134, v143
	v_cndmask_b32_e32 v139, v238, v139, vcc
	v_lshlrev_b32_e32 v142, 2, v139
	ds_bpermute_b32 v143, v142, v134
	v_cmp_eq_u32_e32 vcc, 0, v189
	v_lshl_add_u32 v139, v168, 2, s60
	s_and_saveexec_b64 s[0:1], vcc
	s_cbranch_execz .LBB0_2127
	s_waitcnt lgkmcnt(0)
	v_add_f32_e32 v134, v134, v143
	ds_write_b32 v139, v134

.LBB0_2547:
	s_or_b64 exec, exec, s[0:1]
	v_readlane_b32 s68, v254, 24
	v_lshl_add_u32 v168, v188, 2, s58
	s_cmp_gt_i32 s28, 7
	v_readlane_b32 s78, v254, 34
	v_readlane_b32 s79, v254, 35
	v_readlane_b32 s80, v254, 36
	v_readlane_b32 s81, v254, 37
	v_ashrrev_i32_e32 v169, 31, v168
	v_lshlrev_b32_e32 v138, 8, v154
	s_cselect_b32 s0, s80, s78
	s_cselect_b32 s1, s81, s79
	v_lshlrev_b64 v[172:173], 2, v[168:169]
	v_and_b32_e32 v202, 0x7ff00, v138
	s_waitcnt lgkmcnt(0)
	s_barrier
	s_mov_b64 s[98:99], 0x1000
	s_mov_b64 s[100:101], 0x5000
	v_lshl_add_u64 v[122:123], s[0:1], 0, v[172:173]
	v_lshl_add_u64 v[138:139], s[8:9], 0, v[202:203]
	v_lshl_add_u64 v[142:143], s[16:17], 0, v[202:203]
	global_load_dwordx4 v[126:129], v[122:123], off
	s_waitcnt lgkmcnt(0)
	global_load_dwordx4 v[122:125], v[122:123], off offset:256
	v_lshl_add_u64 v[138:139], v[138:139], 0, v[172:173]
	v_lshl_add_u64 v[142:143], v[142:143], 0, v[172:173]
	v_lshl_add_u64 v[244:245], v[138:139], 0, s[98:99]
	v_lshl_add_u64 v[250:251], v[142:143], 0, s[98:99]
	global_load_dwordx4 v[138:141], v[138:139], off
	s_cselect_b32 s2, 0x800, 0
	global_load_dwordx4 v[142:145], v[142:143], off
	global_load_dwordx4 v[244:247], v[244:245], off
	global_load_dwordx4 v[250:253], v[250:251], off
	s_lshl_b32 s21, s28, 8
	s_and_b32 s21, s21, 0x700
	s_or_b32 s2, s2, s21
	s_add_i32 s21, 0, 0x20000
	v_add_u32_e32 v157, s21, v146
	ds_read_b128 v[146:149], v157
	v_mov_b64_e32 v[176:177], s[6:7]
	v_cvt_f32_i32_e32 v131, v131
	v_cvt_f32_i32_e32 v130, v130
	s_waitcnt lgkmcnt(0)
	v_mov_b32_e32 v150, v147
	v_mov_b32_e32 v151, v148
	v_mov_b32_e32 v147, v149
	v_pk_add_f32 v[146:147], v[150:151], v[146:147]
	v_cvt_f32_i32_e32 v133, v133
	v_add_f32_e32 v146, v146, v147
	v_fmamk_f32 v146, v146, 0x3c000000, v230
	v_cmp_gt_f32_e32 vcc, s63, v146
	v_mul_f32_e32 v147, 0x4f800000, v146
	v_cvt_f32_i32_e32 v132, v132
	v_cndmask_b32_e32 v146, v146, v147, vcc
	v_sqrt_f32_e32 v147, v146
	v_cvt_f32_i32_e32 v137, v137
	v_cvt_f32_i32_e32 v136, v136
	v_cvt_f32_i32_e32 v135, v135
	v_add_u32_e32 v148, -1, v147
	v_fma_f32 v149, -v148, v147, v146
	v_cmp_ge_f32_e64 s[0:1], 0, v149
	v_add_u32_e32 v149, 1, v147
	v_cvt_f32_i32_e32 v134, v134
	v_cndmask_b32_e64 v148, v147, v148, s[0:1]
	v_fma_f32 v147, -v149, v147, v146
	v_cmp_lt_f32_e64 s[0:1], 0, v147
	s_lshl_b32 s2, s2, 1
	v_mov_b64_e32 v[216:217], v[112:113]
	v_cndmask_b32_e64 v147, v148, v149, s[0:1]
	v_mul_f32_e32 v148, 0x37800000, v147
	v_cndmask_b32_e32 v147, v147, v148, vcc
	v_cmp_class_f32_e32 vcc, v146, v231
	v_mad_i64_i32 v[178:179], s[0:1], v154, s64, v[176:177]
	s_nop 0
	v_cndmask_b32_e32 v146, v147, v146, vcc
	v_div_scale_f32 v147, s[0:1], v146, v146, 1.0
	v_rcp_f32_e32 v148, v147
	v_lshl_add_u64 v[192:193], v[178:179], 0, s[2:3]
	v_lshlrev_b64 v[178:179], 1, v[168:169]
	v_lshl_add_u64 v[192:193], v[192:193], 0, v[178:179]
	v_fma_f32 v149, -v147, v148, 1.0
	v_fmac_f32_e32 v148, v149, v148
	v_div_scale_f32 v149, vcc, 1.0, v146, 1.0
	v_mul_f32_e32 v150, v149, v148
	v_fma_f32 v151, -v147, v150, v149
	v_fmac_f32_e32 v150, v151, v148
	v_fma_f32 v147, -v147, v150, v149
	v_div_fmas_f32 v147, v147, v148, v150
	v_div_fixup_f32 v146, v147, v146, 1.0
	v_mul_f32_e32 v146, v156, v146
	v_pk_mul_f32 v[132:133], v[146:147], v[132:133] op_sel_hi:[0,1]
	v_pk_mul_f32 v[130:131], v[146:147], v[130:131] op_sel_hi:[0,1]
	v_pk_mul_f32 v[134:135], v[146:147], v[134:135] op_sel_hi:[0,1]
	v_pk_mul_f32 v[136:137], v[146:147], v[136:137] op_sel_hi:[0,1]
	v_mov_b64_e32 v[214:215], v[110:111]
	s_cmp_lt_i32 s28, 8
	v_readlane_b32 s69, v254, 25
	v_readlane_b32 s70, v254, 26
	v_readlane_b32 s71, v254, 27
	v_readlane_b32 s72, v254, 28
	v_readlane_b32 s73, v254, 29
	v_readlane_b32 s74, v254, 30
	v_readlane_b32 s75, v254, 31
	v_readlane_b32 s76, v254, 32
	s_waitcnt vmcnt(2)
	v_pk_mul_f32 v[136:137], v[128:129], v[136:137]
	v_pk_mul_f32 v[130:131], v[122:123], v[130:131]
	v_pk_mul_f32 v[132:133], v[124:125], v[132:133]
	v_pk_mul_f32 v[134:135], v[126:127], v[134:135]
	v_readlane_b32 s77, v254, 33
	v_readlane_b32 s82, v254, 38
	v_pk_mul_f32 v[146:147], v[144:145], v[132:133]
	v_pk_mul_f32 v[148:149], v[142:143], v[130:131]
	v_pk_fma_f32 v[146:147], v[140:141], v[136:137], v[146:147] neg_lo:[0,0,1] neg_hi:[0,0,1]
	v_pk_fma_f32 v[148:149], v[138:139], v[134:135], v[148:149] neg_lo:[0,0,1] neg_hi:[0,0,1]
	v_pk_mul_f32 v[136:137], v[144:145], v[136:137]
	v_pk_mul_f32 v[134:135], v[142:143], v[134:135]
	v_pk_fma_f32 v[152:153], v[140:141], v[132:133], v[136:137]
	v_pk_fma_f32 v[150:151], v[138:139], v[130:131], v[134:135]
	v_pk_add_f32 v[136:137], v[146:147], 0 op_sel_hi:[1,0]
	v_pk_add_f32 v[134:135], v[148:149], 0 op_sel_hi:[1,0]
	v_pk_add_f32 v[132:133], v[152:153], 0 op_sel_hi:[1,0]
	v_pk_add_f32 v[130:131], v[150:151], 0 op_sel_hi:[1,0]
	v_readlane_b32 s83, v254, 39
	v_cvt_pk_bf16_f32 v148, v148, v149
	v_cvt_pk_bf16_f32 v149, v146, v147
	v_cvt_pk_bf16_f32 v146, v150, v151
	v_cvt_pk_bf16_f32 v147, v152, v153
	global_store_dwordx2 v[192:193], v[148:149], off
	global_store_dwordx2 v[192:193], v[146:147], off offset:128
	ds_read_b128 v[146:149], v157 offset:16
	s_waitcnt lgkmcnt(0)
	v_mov_b32_e32 v150, v147
	v_mov_b32_e32 v151, v148
	v_mov_b32_e32 v147, v149
	v_pk_add_f32 v[146:147], v[150:151], v[146:147]
	s_nop 0
	v_add_f32_e32 v146, v146, v147
	v_fmamk_f32 v146, v146, 0x3c000000, v230
	v_cmp_gt_f32_e32 vcc, s63, v146
	v_mul_f32_e32 v147, 0x4f800000, v146
	s_nop 0
	v_cndmask_b32_e32 v146, v146, v147, vcc
	v_sqrt_f32_e32 v147, v146
	s_nop 0
	v_add_u32_e32 v148, -1, v147
	v_fma_f32 v149, -v148, v147, v146
	v_cmp_ge_f32_e64 s[0:1], 0, v149
	v_add_u32_e32 v149, 1, v147
	s_nop 0
	v_cndmask_b32_e64 v148, v147, v148, s[0:1]
	v_fma_f32 v147, -v149, v147, v146
	v_cmp_lt_f32_e64 s[0:1], 0, v147
	s_nop 1
	v_cndmask_b32_e64 v147, v148, v149, s[0:1]
	v_mul_f32_e32 v148, 0x37800000, v147
	v_cndmask_b32_e32 v147, v147, v148, vcc
	v_cmp_class_f32_e32 vcc, v146, v231
	s_nop 1
	v_cndmask_b32_e32 v146, v147, v146, vcc
	v_div_scale_f32 v147, s[0:1], v146, v146, 1.0
	v_rcp_f32_e32 v148, v147
	s_nop 0
	v_fma_f32 v149, -v147, v148, 1.0
	v_fmac_f32_e32 v148, v149, v148
	v_div_scale_f32 v149, vcc, 1.0, v146, 1.0
	v_mul_f32_e32 v150, v149, v148
	v_fma_f32 v151, -v147, v150, v149
	v_fmac_f32_e32 v150, v151, v148
	v_fma_f32 v147, -v147, v150, v149
	v_div_fmas_f32 v147, v147, v148, v150
	v_div_fixup_f32 v157, v147, v146, 1.0
	v_mov_b64_e32 v[148:149], v[120:121]
	v_mov_b64_e32 v[152:153], v[116:117]
	v_mov_b64_e32 v[146:147], v[118:119]
	v_mov_b64_e32 v[150:151], v[114:115]
	v_mul_f32_e32 v202, v156, v157
	v_cvt_f32_i32_e32 v149, v149
	v_cvt_f32_i32_e32 v148, v148
	v_cvt_f32_i32_e32 v147, v147
	v_cvt_f32_i32_e32 v146, v146
	v_cvt_f32_i32_e32 v151, v151
	v_cvt_f32_i32_e32 v150, v150
	v_cvt_f32_i32_e32 v153, v153
	v_cvt_f32_i32_e32 v152, v152
	v_pk_mul_f32 v[146:147], v[202:203], v[146:147] op_sel_hi:[0,1]
	v_pk_mul_f32 v[148:149], v[202:203], v[148:149] op_sel_hi:[0,1]
	v_pk_mul_f32 v[150:151], v[202:203], v[150:151] op_sel_hi:[0,1]
	v_pk_mul_f32 v[152:153], v[202:203], v[152:153] op_sel_hi:[0,1]
	v_pk_mul_f32 v[148:149], v[128:129], v[148:149]
	v_pk_mul_f32 v[146:147], v[126:127], v[146:147]
	v_pk_mul_f32 v[150:151], v[122:123], v[150:151]
	v_pk_mul_f32 v[152:153], v[124:125], v[152:153]
	v_pk_mul_f32 v[212:213], v[142:143], v[150:151]
	v_pk_mul_f32 v[210:211], v[144:145], v[152:153]
	v_pk_mul_f32 v[144:145], v[144:145], v[148:149]
	v_pk_mul_f32 v[142:143], v[142:143], v[146:147]
	v_pk_fma_f32 v[212:213], v[138:139], v[146:147], v[212:213] neg_lo:[0,0,1] neg_hi:[0,0,1]
	v_pk_fma_f32 v[210:211], v[140:141], v[148:149], v[210:211] neg_lo:[0,0,1] neg_hi:[0,0,1]
	v_pk_fma_f32 v[146:147], v[138:139], v[150:151], v[142:143]
	v_pk_fma_f32 v[148:149], v[140:141], v[152:153], v[144:145]
	v_pk_add_f32 v[144:145], v[210:211], 0 op_sel_hi:[1,0]
	v_pk_add_f32 v[142:143], v[212:213], 0 op_sel_hi:[1,0]
	v_pk_add_f32 v[140:141], v[148:149], 0 op_sel_hi:[1,0]
	v_pk_add_f32 v[138:139], v[146:147], 0 op_sel_hi:[1,0]
	v_add_u32_e32 v157, 16, v190
	v_cvt_pk_bf16_f32 v150, v212, v213
	v_cvt_pk_bf16_f32 v151, v210, v211
	v_cvt_pk_bf16_f32 v146, v146, v147
	v_add_u32_e32 v167, s19, v157
	v_cvt_pk_bf16_f32 v147, v148, v149
	global_store_dwordx2 v[192:193], v[150:151], off offset:256
	global_store_dwordx2 v[192:193], v[146:147], off offset:384
	v_lshlrev_b32_e32 v146, 8, v167
	v_and_b32_e32 v202, 0x7ff00, v146
	v_lshl_add_u64 v[146:147], s[8:9], 0, v[202:203]
	v_lshl_add_u64 v[150:151], s[16:17], 0, v[202:203]
	v_lshl_add_u64 v[146:147], v[146:147], 0, v[172:173]
	v_lshl_add_u64 v[150:151], v[150:151], 0, v[172:173]
	s_waitcnt vmcnt(4)
	v_mov_b32_e32 v148, v246
	v_mov_b32_e32 v149, v247
	v_lshl_add_u64 v[246:247], v[146:147], 0, s[98:99]
	v_mov_b32_e32 v146, v244
	v_mov_b32_e32 v147, v245
	global_load_dwordx4 v[244:247], v[246:247], off
	v_lshl_add_u32 v157, v157, 5, s21
	v_mov_b32_e32 v152, v252
	v_mov_b32_e32 v153, v253
	v_lshl_add_u64 v[252:253], v[150:151], 0, s[98:99]
	v_mov_b32_e32 v150, v250
	v_mov_b32_e32 v151, v251
	global_load_dwordx4 v[250:253], v[252:253], off
	ds_read_b128 v[210:213], v157
	s_waitcnt lgkmcnt(0)
	v_mov_b32_e32 v192, v211
	v_mov_b32_e32 v193, v212
	v_mov_b32_e32 v211, v213
	v_pk_add_f32 v[192:193], v[192:193], v[210:211]
	v_mov_b64_e32 v[212:213], v[108:109]
	v_add_f32_e32 v169, v192, v193
	v_fmamk_f32 v169, v169, 0x3c000000, v230
	v_cmp_gt_f32_e32 vcc, s63, v169
	v_mul_f32_e32 v171, 0x4f800000, v169
	v_mov_b64_e32 v[210:211], v[106:107]
	v_cndmask_b32_e32 v169, v169, v171, vcc
	v_sqrt_f32_e32 v171, v169
	s_nop 0
	v_cvt_f32_i32_e32 v211, v211
	v_add_u32_e32 v175, -1, v171
	v_fma_f32 v181, -v175, v171, v169
	v_cmp_ge_f32_e64 s[0:1], 0, v181
	v_add_u32_e32 v181, 1, v171
	v_cvt_f32_i32_e32 v210, v210
	v_cndmask_b32_e64 v175, v171, v175, s[0:1]
	v_fma_f32 v171, -v181, v171, v169
	v_cmp_lt_f32_e64 s[0:1], 0, v171
	v_cvt_f32_i32_e32 v213, v213
	v_cvt_f32_i32_e32 v212, v212
	v_cndmask_b32_e64 v171, v175, v181, s[0:1]
	v_mul_f32_e32 v175, 0x37800000, v171
	v_cndmask_b32_e32 v171, v171, v175, vcc
	v_cmp_class_f32_e32 vcc, v169, v231
	v_cvt_f32_i32_e32 v193, v217
	v_cvt_f32_i32_e32 v192, v216
	v_cndmask_b32_e32 v169, v171, v169, vcc
	v_div_scale_f32 v171, s[0:1], v169, v169, 1.0
	v_rcp_f32_e32 v175, v171
	v_cvt_f32_i32_e32 v215, v215
	v_cvt_f32_i32_e32 v214, v214
	v_fma_f32 v181, -v171, v175, 1.0
	v_fmac_f32_e32 v175, v181, v175
	v_div_scale_f32 v181, vcc, 1.0, v169, 1.0
	v_mul_f32_e32 v183, v181, v175
	v_fma_f32 v185, -v171, v183, v181
	v_fmac_f32_e32 v183, v185, v175
	v_fma_f32 v171, -v171, v183, v181
	v_div_fmas_f32 v171, v171, v175, v183
	v_div_fixup_f32 v169, v171, v169, 1.0
	v_mul_f32_e32 v202, v186, v169
	v_pk_mul_f32 v[212:213], v[202:203], v[212:213] op_sel_hi:[0,1]
	v_pk_mul_f32 v[210:211], v[202:203], v[210:211] op_sel_hi:[0,1]
	v_pk_mul_f32 v[214:215], v[202:203], v[214:215] op_sel_hi:[0,1]
	v_pk_mul_f32 v[192:193], v[202:203], v[192:193] op_sel_hi:[0,1]
	v_pk_mul_f32 v[210:211], v[122:123], v[210:211]
	v_pk_mul_f32 v[212:213], v[124:125], v[212:213]
	v_pk_mul_f32 v[192:193], v[128:129], v[192:193]
	v_pk_mul_f32 v[214:215], v[126:127], v[214:215]
	v_pk_mul_f32 v[216:217], v[152:153], v[212:213]
	v_pk_mul_f32 v[236:237], v[150:151], v[210:211]
	v_pk_fma_f32 v[216:217], v[148:149], v[192:193], v[216:217] neg_lo:[0,0,1] neg_hi:[0,0,1]
	v_pk_fma_f32 v[236:237], v[146:147], v[214:215], v[236:237] neg_lo:[0,0,1] neg_hi:[0,0,1]
	v_pk_mul_f32 v[192:193], v[152:153], v[192:193]
	v_pk_mul_f32 v[214:215], v[150:151], v[214:215]
	v_pk_fma_f32 v[192:193], v[148:149], v[212:213], v[192:193]
	v_pk_fma_f32 v[210:211], v[146:147], v[210:211], v[214:215]
	v_mad_i64_i32 v[212:213], s[0:1], v167, s64, v[176:177]
	v_pk_add_f32 v[136:137], v[136:137], v[216:217]
	v_pk_add_f32 v[134:135], v[134:135], v[236:237]
	v_pk_add_f32 v[132:133], v[132:133], v[192:193]
	v_pk_add_f32 v[130:131], v[130:131], v[210:211]
	v_lshl_add_u64 v[212:213], v[212:213], 0, s[2:3]
	v_lshl_add_u64 v[238:239], v[212:213], 0, v[178:179]
	v_cvt_pk_bf16_f32 v212, v236, v237
	v_cvt_pk_bf16_f32 v213, v216, v217
	v_cvt_pk_bf16_f32 v210, v210, v211
	v_cvt_pk_bf16_f32 v211, v192, v193
	global_store_dwordx2 v[238:239], v[212:213], off
	global_store_dwordx2 v[238:239], v[210:211], off offset:128
	ds_read_b128 v[210:213], v157 offset:16
	v_mov_b64_e32 v[216:217], v[104:105]
	v_mov_b64_e32 v[214:215], v[102:103]
	s_waitcnt lgkmcnt(0)
	v_mov_b32_e32 v192, v211
	v_mov_b32_e32 v193, v212
	v_mov_b32_e32 v211, v213
	v_pk_add_f32 v[192:193], v[192:193], v[210:211]
	v_mov_b64_e32 v[212:213], v[100:101]
	v_add_f32_e32 v157, v192, v193
	v_fmamk_f32 v157, v157, 0x3c000000, v230
	v_cmp_gt_f32_e32 vcc, s63, v157
	v_mul_f32_e32 v167, 0x4f800000, v157
	v_mov_b64_e32 v[210:211], v[98:99]
	v_cndmask_b32_e32 v157, v157, v167, vcc
	v_sqrt_f32_e32 v167, v157
	s_nop 0
	v_cvt_f32_i32_e32 v193, v217
	v_add_u32_e32 v169, -1, v167
	v_fma_f32 v171, -v169, v167, v157
	v_cmp_ge_f32_e64 s[0:1], 0, v171
	v_add_u32_e32 v171, 1, v167
	v_cvt_f32_i32_e32 v192, v216
	v_cndmask_b32_e64 v169, v167, v169, s[0:1]
	v_fma_f32 v167, -v171, v167, v157
	v_cmp_lt_f32_e64 s[0:1], 0, v167
	v_cvt_f32_i32_e32 v215, v215
	v_cvt_f32_i32_e32 v214, v214
	v_cndmask_b32_e64 v167, v169, v171, s[0:1]
	v_mul_f32_e32 v169, 0x37800000, v167
	v_cndmask_b32_e32 v167, v167, v169, vcc
	v_cmp_class_f32_e32 vcc, v157, v231
	v_cvt_f32_i32_e32 v211, v211
	v_cvt_f32_i32_e32 v210, v210
	v_cndmask_b32_e32 v157, v167, v157, vcc
	v_div_scale_f32 v167, s[0:1], v157, v157, 1.0
	v_rcp_f32_e32 v169, v167
	v_cvt_f32_i32_e32 v213, v213
	v_cvt_f32_i32_e32 v212, v212
	v_fma_f32 v171, -v167, v169, 1.0
	v_fmac_f32_e32 v169, v171, v169
	v_div_scale_f32 v171, vcc, 1.0, v157, 1.0
	v_mul_f32_e32 v175, v171, v169
	v_fma_f32 v181, -v167, v175, v171
	v_fmac_f32_e32 v175, v181, v169
	v_fma_f32 v167, -v167, v175, v171
	v_div_fmas_f32 v167, v167, v169, v175
	v_div_fixup_f32 v157, v167, v157, 1.0
	v_mul_f32_e32 v186, v186, v157
	v_pk_mul_f32 v[214:215], v[186:187], v[214:215] op_sel_hi:[0,1]
	v_pk_mul_f32 v[192:193], v[186:187], v[192:193] op_sel_hi:[0,1]
	v_pk_mul_f32 v[212:213], v[186:187], v[212:213] op_sel_hi:[0,1]
	v_pk_mul_f32 v[186:187], v[186:187], v[210:211] op_sel_hi:[0,1]
	v_pk_mul_f32 v[192:193], v[128:129], v[192:193]
	v_pk_mul_f32 v[214:215], v[126:127], v[214:215]
	v_pk_mul_f32 v[186:187], v[122:123], v[186:187]
	v_pk_mul_f32 v[210:211], v[124:125], v[212:213]
	v_pk_mul_f32 v[216:217], v[150:151], v[186:187]
	v_pk_mul_f32 v[212:213], v[152:153], v[210:211]
	v_pk_mul_f32 v[152:153], v[152:153], v[192:193]
	v_pk_mul_f32 v[150:151], v[150:151], v[214:215]
	v_pk_fma_f32 v[216:217], v[146:147], v[214:215], v[216:217] neg_lo:[0,0,1] neg_hi:[0,0,1]
	v_pk_fma_f32 v[212:213], v[148:149], v[192:193], v[212:213] neg_lo:[0,0,1] neg_hi:[0,0,1]
	v_pk_fma_f32 v[146:147], v[146:147], v[186:187], v[150:151]
	v_pk_fma_f32 v[148:149], v[148:149], v[210:211], v[152:153]
	v_pk_add_f32 v[144:145], v[144:145], v[212:213]
	v_pk_add_f32 v[142:143], v[142:143], v[216:217]
	v_pk_add_f32 v[140:141], v[140:141], v[148:149]
	v_pk_add_f32 v[138:139], v[138:139], v[146:147]
	v_add_u32_e32 v157, 32, v190
	v_cvt_pk_bf16_f32 v150, v216, v217
	v_cvt_pk_bf16_f32 v151, v212, v213
	v_cvt_pk_bf16_f32 v146, v146, v147
	v_add_u32_e32 v167, s19, v157
	v_cvt_pk_bf16_f32 v147, v148, v149
	global_store_dwordx2 v[238:239], v[150:151], off offset:256
	global_store_dwordx2 v[238:239], v[146:147], off offset:384
	v_lshlrev_b32_e32 v146, 8, v167
	v_and_b32_e32 v202, 0x7ff00, v146
	v_lshl_add_u64 v[146:147], s[8:9], 0, v[202:203]
	v_lshl_add_u64 v[150:151], s[16:17], 0, v[202:203]
	v_lshl_add_u64 v[146:147], v[146:147], 0, v[172:173]
	v_lshl_add_u64 v[150:151], v[150:151], 0, v[172:173]
	s_waitcnt vmcnt(4)
	v_mov_b32_e32 v148, v246
	v_mov_b32_e32 v149, v247
	v_lshl_add_u64 v[246:247], v[146:147], 0, s[98:99]
	v_mov_b32_e32 v146, v244
	v_mov_b32_e32 v147, v245
	global_load_dwordx4 v[244:247], v[246:247], off
	v_lshl_add_u32 v157, v157, 5, s21
	v_mov_b32_e32 v152, v252
	v_mov_b32_e32 v153, v253
	v_lshl_add_u64 v[252:253], v[150:151], 0, s[98:99]
	v_mov_b32_e32 v150, v250
	v_mov_b32_e32 v151, v251
	global_load_dwordx4 v[250:253], v[252:253], off
	ds_read_b128 v[210:213], v157
	v_mov_b64_e32 v[216:217], v[92:93]
	v_mov_b64_e32 v[214:215], v[90:91]
	s_waitcnt lgkmcnt(0)
	v_mov_b32_e32 v186, v211
	v_mov_b32_e32 v187, v212
	v_mov_b32_e32 v211, v213
	v_pk_add_f32 v[186:187], v[186:187], v[210:211]
	v_mov_b64_e32 v[212:213], v[96:97]
	v_add_f32_e32 v169, v186, v187
	v_fmamk_f32 v169, v169, 0x3c000000, v230
	v_cmp_gt_f32_e32 vcc, s63, v169
	v_mul_f32_e32 v171, 0x4f800000, v169
	v_mov_b64_e32 v[210:211], v[94:95]
	v_cndmask_b32_e32 v169, v169, v171, vcc
	v_sqrt_f32_e32 v171, v169
	s_nop 0
	v_cvt_f32_i32_e32 v187, v213
	v_add_u32_e32 v175, -1, v171
	v_fma_f32 v181, -v175, v171, v169
	v_cmp_ge_f32_e64 s[0:1], 0, v181
	v_add_u32_e32 v181, 1, v171
	v_cvt_f32_i32_e32 v186, v212
	v_cndmask_b32_e64 v175, v171, v175, s[0:1]
	v_fma_f32 v171, -v181, v171, v169
	v_cmp_lt_f32_e64 s[0:1], 0, v171
	v_cvt_f32_i32_e32 v193, v211
	v_cvt_f32_i32_e32 v192, v210
	v_cndmask_b32_e64 v171, v175, v181, s[0:1]
	v_mul_f32_e32 v175, 0x37800000, v171
	v_cndmask_b32_e32 v171, v171, v175, vcc
	v_cmp_class_f32_e32 vcc, v169, v231
	v_cvt_f32_i32_e32 v211, v215
	v_cvt_f32_i32_e32 v210, v214
	v_cndmask_b32_e32 v169, v171, v169, vcc
	v_div_scale_f32 v171, s[0:1], v169, v169, 1.0
	v_rcp_f32_e32 v175, v171
	v_cvt_f32_i32_e32 v213, v217
	v_cvt_f32_i32_e32 v212, v216
	v_fma_f32 v181, -v171, v175, 1.0
	v_fmac_f32_e32 v175, v181, v175
	v_div_scale_f32 v181, vcc, 1.0, v169, 1.0
	v_mul_f32_e32 v183, v181, v175
	v_fma_f32 v185, -v171, v183, v181
	v_fmac_f32_e32 v183, v185, v175
	v_fma_f32 v171, -v171, v183, v181
	v_div_fmas_f32 v171, v171, v175, v183
	v_div_fixup_f32 v169, v171, v169, 1.0
	v_mul_f32_e32 v202, v184, v169
	v_pk_mul_f32 v[212:213], v[202:203], v[212:213] op_sel_hi:[0,1]
	v_pk_mul_f32 v[210:211], v[202:203], v[210:211] op_sel_hi:[0,1]
	v_pk_mul_f32 v[192:193], v[202:203], v[192:193] op_sel_hi:[0,1]
	v_pk_mul_f32 v[186:187], v[202:203], v[186:187] op_sel_hi:[0,1]
	v_pk_mul_f32 v[210:211], v[122:123], v[210:211]
	v_pk_mul_f32 v[212:213], v[124:125], v[212:213]
	v_pk_mul_f32 v[186:187], v[128:129], v[186:187]
	v_pk_mul_f32 v[192:193], v[126:127], v[192:193]
	v_pk_mul_f32 v[214:215], v[152:153], v[212:213]
	v_pk_mul_f32 v[216:217], v[150:151], v[210:211]
	v_pk_fma_f32 v[214:215], v[148:149], v[186:187], v[214:215] neg_lo:[0,0,1] neg_hi:[0,0,1]
	v_pk_fma_f32 v[216:217], v[146:147], v[192:193], v[216:217] neg_lo:[0,0,1] neg_hi:[0,0,1]
	v_pk_mul_f32 v[186:187], v[152:153], v[186:187]
	v_pk_mul_f32 v[192:193], v[150:151], v[192:193]
	v_pk_fma_f32 v[186:187], v[148:149], v[212:213], v[186:187]
	v_pk_fma_f32 v[192:193], v[146:147], v[210:211], v[192:193]
	v_mad_i64_i32 v[210:211], s[0:1], v167, s64, v[176:177]
	v_pk_add_f32 v[136:137], v[136:137], v[214:215]
	v_pk_add_f32 v[134:135], v[134:135], v[216:217]
	v_pk_add_f32 v[132:133], v[132:133], v[186:187]
	v_pk_add_f32 v[130:131], v[130:131], v[192:193]
	v_lshl_add_u64 v[210:211], v[210:211], 0, s[2:3]
	v_lshl_add_u64 v[236:237], v[210:211], 0, v[178:179]
	v_cvt_pk_bf16_f32 v210, v216, v217
	v_cvt_pk_bf16_f32 v211, v214, v215
	v_cvt_pk_bf16_f32 v192, v192, v193
	v_cvt_pk_bf16_f32 v193, v186, v187
	global_store_dwordx2 v[236:237], v[210:211], off
	global_store_dwordx2 v[236:237], v[192:193], off offset:128
	ds_read_b128 v[210:213], v157 offset:16
	v_mov_b64_e32 v[216:217], v[88:89]
	v_mov_b64_e32 v[214:215], v[86:87]
	s_waitcnt lgkmcnt(0)
	v_mov_b32_e32 v186, v211
	v_mov_b32_e32 v187, v212
	v_mov_b32_e32 v211, v213
	v_pk_add_f32 v[186:187], v[186:187], v[210:211]
	v_mov_b64_e32 v[212:213], v[84:85]
	v_add_f32_e32 v157, v186, v187
	v_fmamk_f32 v157, v157, 0x3c000000, v230
	v_cmp_gt_f32_e32 vcc, s63, v157
	v_mul_f32_e32 v167, 0x4f800000, v157
	v_mov_b64_e32 v[210:211], v[82:83]
	v_cndmask_b32_e32 v157, v157, v167, vcc
	v_sqrt_f32_e32 v167, v157
	s_nop 0
	v_cvt_f32_i32_e32 v187, v217
	v_add_u32_e32 v169, -1, v167
	v_fma_f32 v171, -v169, v167, v157
	v_cmp_ge_f32_e64 s[0:1], 0, v171
	v_add_u32_e32 v171, 1, v167
	v_cvt_f32_i32_e32 v186, v216
	v_cndmask_b32_e64 v169, v167, v169, s[0:1]
	v_fma_f32 v167, -v171, v167, v157
	v_cmp_lt_f32_e64 s[0:1], 0, v167
	v_cvt_f32_i32_e32 v193, v215
	v_cvt_f32_i32_e32 v192, v214
	v_cndmask_b32_e64 v167, v169, v171, s[0:1]
	v_mul_f32_e32 v169, 0x37800000, v167
	v_cndmask_b32_e32 v167, v167, v169, vcc
	v_cmp_class_f32_e32 vcc, v157, v231
	v_cvt_f32_i32_e32 v211, v211
	v_cvt_f32_i32_e32 v210, v210
	v_cndmask_b32_e32 v157, v167, v157, vcc
	v_div_scale_f32 v167, s[0:1], v157, v157, 1.0
	v_rcp_f32_e32 v169, v167
	v_cvt_f32_i32_e32 v213, v213
	v_cvt_f32_i32_e32 v212, v212
	v_fma_f32 v171, -v167, v169, 1.0
	v_fmac_f32_e32 v169, v171, v169
	v_div_scale_f32 v171, vcc, 1.0, v157, 1.0
	v_mul_f32_e32 v175, v171, v169
	v_fma_f32 v181, -v167, v175, v171
	v_fmac_f32_e32 v175, v181, v169
	v_fma_f32 v167, -v167, v175, v171
	v_div_fmas_f32 v167, v167, v169, v175
	v_div_fixup_f32 v157, v167, v157, 1.0
	v_mul_f32_e32 v184, v184, v157
	v_pk_mul_f32 v[192:193], v[184:185], v[192:193] op_sel_hi:[0,1]
	v_pk_mul_f32 v[186:187], v[184:185], v[186:187] op_sel_hi:[0,1]
	v_pk_mul_f32 v[212:213], v[184:185], v[212:213] op_sel_hi:[0,1]
	v_pk_mul_f32 v[184:185], v[184:185], v[210:211] op_sel_hi:[0,1]
	v_pk_mul_f32 v[186:187], v[128:129], v[186:187]
	v_pk_mul_f32 v[192:193], v[126:127], v[192:193]
	v_pk_mul_f32 v[184:185], v[122:123], v[184:185]
	v_pk_mul_f32 v[210:211], v[124:125], v[212:213]
	v_pk_mul_f32 v[214:215], v[150:151], v[184:185]
	v_pk_mul_f32 v[212:213], v[152:153], v[210:211]
	v_pk_mul_f32 v[152:153], v[152:153], v[186:187]
	v_pk_mul_f32 v[150:151], v[150:151], v[192:193]
	v_pk_fma_f32 v[214:215], v[146:147], v[192:193], v[214:215] neg_lo:[0,0,1] neg_hi:[0,0,1]
	v_pk_fma_f32 v[212:213], v[148:149], v[186:187], v[212:213] neg_lo:[0,0,1] neg_hi:[0,0,1]
	v_pk_fma_f32 v[146:147], v[146:147], v[184:185], v[150:151]
	v_pk_fma_f32 v[148:149], v[148:149], v[210:211], v[152:153]
	v_pk_add_f32 v[144:145], v[144:145], v[212:213]
	v_pk_add_f32 v[142:143], v[142:143], v[214:215]
	v_pk_add_f32 v[140:141], v[140:141], v[148:149]
	v_pk_add_f32 v[138:139], v[138:139], v[146:147]
	v_add_u32_e32 v157, 48, v190
	v_cvt_pk_bf16_f32 v150, v214, v215
	v_cvt_pk_bf16_f32 v151, v212, v213
	v_cvt_pk_bf16_f32 v146, v146, v147
	v_add_u32_e32 v167, s19, v157
	v_cvt_pk_bf16_f32 v147, v148, v149
	global_store_dwordx2 v[236:237], v[150:151], off offset:256
	global_store_dwordx2 v[236:237], v[146:147], off offset:384
	v_lshlrev_b32_e32 v146, 8, v167
	v_and_b32_e32 v202, 0x7ff00, v146
	v_lshl_add_u64 v[146:147], s[8:9], 0, v[202:203]
	v_lshl_add_u64 v[150:151], s[16:17], 0, v[202:203]
	v_lshl_add_u64 v[146:147], v[146:147], 0, v[172:173]
	v_lshl_add_u64 v[150:151], v[150:151], 0, v[172:173]
	s_waitcnt vmcnt(4)
	v_mov_b32_e32 v148, v246
	v_mov_b32_e32 v149, v247
	v_lshl_add_u64 v[246:247], v[146:147], 0, s[100:101]
	v_mov_b32_e32 v146, v244
	v_mov_b32_e32 v147, v245
	global_load_dwordx4 v[244:247], v[246:247], off
	v_lshl_add_u32 v157, v157, 5, s21
	v_mov_b32_e32 v152, v252
	v_mov_b32_e32 v153, v253
	v_lshl_add_u64 v[252:253], v[150:151], 0, s[100:101]
	v_mov_b32_e32 v150, v250
	v_mov_b32_e32 v151, v251
	global_load_dwordx4 v[250:253], v[252:253], off
	ds_read_b128 v[184:187], v157
	v_mov_b64_e32 v[212:213], v[76:77]
	v_mov_b64_e32 v[210:211], v[74:75]
	s_waitcnt lgkmcnt(0)
	v_mov_b32_e32 v192, v185
	v_mov_b32_e32 v193, v186
	v_mov_b32_e32 v185, v187
	v_pk_add_f32 v[184:185], v[192:193], v[184:185]
	s_nop 0
	v_add_f32_e32 v169, v184, v185
	v_fmamk_f32 v169, v169, 0x3c000000, v230
	v_cmp_gt_f32_e32 vcc, s63, v169
	v_mul_f32_e32 v171, 0x4f800000, v169
	s_nop 0
	v_cndmask_b32_e32 v169, v169, v171, vcc
	v_sqrt_f32_e32 v171, v169
	s_nop 0
	v_add_u32_e32 v175, -1, v171
	v_fma_f32 v181, -v175, v171, v169
	v_cmp_ge_f32_e64 s[0:1], 0, v181
	v_add_u32_e32 v181, 1, v171
	s_nop 0
	v_cndmask_b32_e64 v175, v171, v175, s[0:1]
	v_fma_f32 v171, -v181, v171, v169
	v_cmp_lt_f32_e64 s[0:1], 0, v171
	s_nop 1
	v_cndmask_b32_e64 v171, v175, v181, s[0:1]
	v_mul_f32_e32 v175, 0x37800000, v171
	v_cndmask_b32_e32 v171, v171, v175, vcc
	v_cmp_class_f32_e32 vcc, v169, v231
	s_nop 1
	v_cndmask_b32_e32 v169, v171, v169, vcc
	v_div_scale_f32 v171, s[0:1], v169, v169, 1.0
	v_rcp_f32_e32 v175, v171
	s_nop 0
	v_fma_f32 v181, -v171, v175, 1.0
	v_fmac_f32_e32 v175, v181, v175
	v_div_scale_f32 v181, vcc, 1.0, v169, 1.0
	v_mul_f32_e32 v183, v181, v175
	v_fma_f32 v184, -v171, v183, v181
	v_fmac_f32_e32 v183, v184, v175
	v_mov_b64_e32 v[186:187], v[80:81]
	v_mov_b64_e32 v[184:185], v[78:79]
	v_fma_f32 v171, -v171, v183, v181
	v_cvt_f32_i32_e32 v187, v187
	v_cvt_f32_i32_e32 v186, v186
	v_cvt_f32_i32_e32 v185, v185
	v_cvt_f32_i32_e32 v184, v184
	v_cvt_f32_i32_e32 v211, v211
	v_cvt_f32_i32_e32 v210, v210
	v_cvt_f32_i32_e32 v213, v213
	v_cvt_f32_i32_e32 v212, v212
	v_div_fmas_f32 v171, v171, v175, v183
	v_div_fixup_f32 v169, v171, v169, 1.0
	v_mul_f32_e32 v192, v182, v169
	v_pk_mul_f32 v[184:185], v[192:193], v[184:185] op_sel_hi:[0,1]
	v_pk_mul_f32 v[186:187], v[192:193], v[186:187] op_sel_hi:[0,1]
	v_pk_mul_f32 v[212:213], v[192:193], v[212:213] op_sel_hi:[0,1]
	v_pk_mul_f32 v[192:193], v[192:193], v[210:211] op_sel_hi:[0,1]
	v_pk_mul_f32 v[192:193], v[122:123], v[192:193]
	v_pk_mul_f32 v[210:211], v[124:125], v[212:213]
	v_pk_mul_f32 v[186:187], v[128:129], v[186:187]
	v_pk_mul_f32 v[184:185], v[126:127], v[184:185]
	v_pk_mul_f32 v[212:213], v[152:153], v[210:211]
	v_pk_mul_f32 v[214:215], v[150:151], v[192:193]
	v_pk_fma_f32 v[212:213], v[148:149], v[186:187], v[212:213] neg_lo:[0,0,1] neg_hi:[0,0,1]
	v_pk_fma_f32 v[214:215], v[146:147], v[184:185], v[214:215] neg_lo:[0,0,1] neg_hi:[0,0,1]
	v_pk_mul_f32 v[186:187], v[152:153], v[186:187]
	v_pk_mul_f32 v[184:185], v[150:151], v[184:185]
	v_pk_fma_f32 v[186:187], v[148:149], v[210:211], v[186:187]
	v_pk_fma_f32 v[184:185], v[146:147], v[192:193], v[184:185]
	v_mad_i64_i32 v[192:193], s[0:1], v167, s64, v[176:177]
	v_pk_add_f32 v[136:137], v[136:137], v[212:213]
	v_pk_add_f32 v[134:135], v[134:135], v[214:215]
	v_pk_add_f32 v[132:133], v[132:133], v[186:187]
	v_pk_add_f32 v[130:131], v[130:131], v[184:185]
	v_lshl_add_u64 v[192:193], v[192:193], 0, s[2:3]
	v_lshl_add_u64 v[192:193], v[192:193], 0, v[178:179]
	v_cvt_pk_bf16_f32 v210, v214, v215
	v_cvt_pk_bf16_f32 v211, v212, v213
	v_cvt_pk_bf16_f32 v184, v184, v185
	v_cvt_pk_bf16_f32 v185, v186, v187
	global_store_dwordx2 v[192:193], v[210:211], off
	global_store_dwordx2 v[192:193], v[184:185], off offset:128
	ds_read_b128 v[184:187], v157 offset:16
	s_waitcnt lgkmcnt(0)
	v_mov_b32_e32 v210, v185
	v_mov_b32_e32 v211, v186
	v_mov_b32_e32 v185, v187
	v_pk_add_f32 v[184:185], v[210:211], v[184:185]
	v_mov_b64_e32 v[212:213], v[72:73]
	v_add_f32_e32 v157, v184, v185
	v_fmamk_f32 v157, v157, 0x3c000000, v230
	v_cmp_gt_f32_e32 vcc, s63, v157
	v_mul_f32_e32 v167, 0x4f800000, v157
	v_mov_b64_e32 v[186:187], v[68:69]
	v_cndmask_b32_e32 v157, v157, v167, vcc
	v_sqrt_f32_e32 v167, v157
	v_mov_b64_e32 v[184:185], v[66:67]
	v_mov_b64_e32 v[210:211], v[70:71]
	v_add_u32_e32 v169, -1, v167
	v_fma_f32 v171, -v169, v167, v157
	v_cmp_ge_f32_e64 s[0:1], 0, v171
	v_add_u32_e32 v171, 1, v167
	v_cvt_f32_i32_e32 v213, v213
	v_cndmask_b32_e64 v169, v167, v169, s[0:1]
	v_fma_f32 v167, -v171, v167, v157
	v_cmp_lt_f32_e64 s[0:1], 0, v167
	v_cvt_f32_i32_e32 v212, v212
	v_cvt_f32_i32_e32 v211, v211
	v_cndmask_b32_e64 v167, v169, v171, s[0:1]
	v_mul_f32_e32 v169, 0x37800000, v167
	v_cndmask_b32_e32 v167, v167, v169, vcc
	v_cmp_class_f32_e32 vcc, v157, v231
	v_cvt_f32_i32_e32 v210, v210
	v_cvt_f32_i32_e32 v185, v185
	v_cndmask_b32_e32 v157, v167, v157, vcc
	v_div_scale_f32 v167, s[0:1], v157, v157, 1.0
	v_rcp_f32_e32 v169, v167
	v_cvt_f32_i32_e32 v184, v184
	v_cvt_f32_i32_e32 v187, v187
	v_cvt_f32_i32_e32 v186, v186
	v_fma_f32 v171, -v167, v169, 1.0
	v_fmac_f32_e32 v169, v171, v169
	v_div_scale_f32 v171, vcc, 1.0, v157, 1.0
	v_mul_f32_e32 v175, v171, v169
	v_fma_f32 v181, -v167, v175, v171
	v_fmac_f32_e32 v175, v181, v169
	v_fma_f32 v167, -v167, v175, v171
	v_div_fmas_f32 v167, v167, v169, v175
	v_div_fixup_f32 v157, v167, v157, 1.0
	v_mul_f32_e32 v182, v182, v157
	v_pk_mul_f32 v[210:211], v[182:183], v[210:211] op_sel_hi:[0,1]
	v_pk_mul_f32 v[212:213], v[182:183], v[212:213] op_sel_hi:[0,1]
	v_pk_mul_f32 v[186:187], v[182:183], v[186:187] op_sel_hi:[0,1]
	v_pk_mul_f32 v[182:183], v[182:183], v[184:185] op_sel_hi:[0,1]
	v_pk_mul_f32 v[212:213], v[128:129], v[212:213]
	v_pk_mul_f32 v[210:211], v[126:127], v[210:211]
	v_pk_mul_f32 v[182:183], v[122:123], v[182:183]
	v_pk_mul_f32 v[184:185], v[124:125], v[186:187]
	v_pk_mul_f32 v[214:215], v[150:151], v[182:183]
	v_pk_mul_f32 v[186:187], v[152:153], v[184:185]
	v_pk_mul_f32 v[152:153], v[152:153], v[212:213]
	v_pk_mul_f32 v[150:151], v[150:151], v[210:211]
	v_pk_fma_f32 v[214:215], v[146:147], v[210:211], v[214:215] neg_lo:[0,0,1] neg_hi:[0,0,1]
	v_pk_fma_f32 v[186:187], v[148:149], v[212:213], v[186:187] neg_lo:[0,0,1] neg_hi:[0,0,1]
	v_pk_fma_f32 v[146:147], v[146:147], v[182:183], v[150:151]
	v_pk_fma_f32 v[148:149], v[148:149], v[184:185], v[152:153]
	v_pk_add_f32 v[144:145], v[144:145], v[186:187]
	v_pk_add_f32 v[142:143], v[142:143], v[214:215]
	v_pk_add_f32 v[140:141], v[140:141], v[148:149]
	v_pk_add_f32 v[138:139], v[138:139], v[146:147]
	v_add_u32_e32 v157, 0x80, v190
	v_cvt_pk_bf16_f32 v150, v214, v215
	v_cvt_pk_bf16_f32 v151, v186, v187
	v_cvt_pk_bf16_f32 v146, v146, v147
	v_add_u32_e32 v167, s19, v157
	v_cvt_pk_bf16_f32 v147, v148, v149
	global_store_dwordx2 v[192:193], v[150:151], off offset:256
	global_store_dwordx2 v[192:193], v[146:147], off offset:384
	v_lshlrev_b32_e32 v146, 8, v167
	v_and_b32_e32 v202, 0x7ff00, v146
	v_lshl_add_u64 v[146:147], s[8:9], 0, v[202:203]
	v_lshl_add_u64 v[150:151], s[16:17], 0, v[202:203]
	v_lshl_add_u64 v[146:147], v[146:147], 0, v[172:173]
	v_lshl_add_u64 v[150:151], v[150:151], 0, v[172:173]
	s_waitcnt vmcnt(4)
	v_mov_b32_e32 v148, v246
	v_mov_b32_e32 v149, v247
	v_lshl_add_u64 v[246:247], v[146:147], 0, s[98:99]
	v_mov_b32_e32 v146, v244
	v_mov_b32_e32 v147, v245
	global_load_dwordx4 v[244:247], v[246:247], off
	v_lshl_add_u32 v157, v157, 5, s21
	v_mov_b32_e32 v152, v252
	v_mov_b32_e32 v153, v253
	v_lshl_add_u64 v[252:253], v[150:151], 0, s[98:99]
	v_mov_b32_e32 v150, v250
	v_mov_b32_e32 v151, v251
	global_load_dwordx4 v[250:253], v[252:253], off
	ds_read_b128 v[182:185], v157
	v_mov_b64_e32 v[212:213], v[60:61]
	v_mov_b64_e32 v[210:211], v[58:59]
	s_waitcnt lgkmcnt(0)
	v_mov_b32_e32 v186, v183
	v_mov_b32_e32 v187, v184
	v_mov_b32_e32 v183, v185
	v_pk_add_f32 v[182:183], v[186:187], v[182:183]
	s_nop 0
	v_add_f32_e32 v169, v182, v183
	v_fmamk_f32 v169, v169, 0x3c000000, v230
	v_cmp_gt_f32_e32 vcc, s63, v169
	v_mul_f32_e32 v171, 0x4f800000, v169
	s_nop 0
	v_cndmask_b32_e32 v169, v169, v171, vcc
	v_sqrt_f32_e32 v171, v169
	s_nop 0
	v_add_u32_e32 v175, -1, v171
	v_fma_f32 v181, -v175, v171, v169
	v_cmp_ge_f32_e64 s[0:1], 0, v181
	v_add_u32_e32 v181, 1, v171
	s_nop 0
	v_cndmask_b32_e64 v175, v171, v175, s[0:1]
	v_fma_f32 v171, -v181, v171, v169
	v_cmp_lt_f32_e64 s[0:1], 0, v171
	s_nop 1
	v_cndmask_b32_e64 v171, v175, v181, s[0:1]
	v_mul_f32_e32 v175, 0x37800000, v171
	v_cndmask_b32_e32 v171, v171, v175, vcc
	v_cmp_class_f32_e32 vcc, v169, v231
	s_nop 1
	v_cndmask_b32_e32 v169, v171, v169, vcc
	v_div_scale_f32 v171, s[0:1], v169, v169, 1.0
	v_rcp_f32_e32 v175, v171
	s_nop 0
	v_fma_f32 v181, -v171, v175, 1.0
	v_fmac_f32_e32 v175, v181, v175
	v_div_scale_f32 v181, vcc, 1.0, v169, 1.0
	v_mul_f32_e32 v182, v181, v175
	v_fma_f32 v183, -v171, v182, v181
	v_fmac_f32_e32 v182, v183, v175
	v_fma_f32 v171, -v171, v182, v181
	v_div_fmas_f32 v171, v171, v175, v182
	v_mov_b64_e32 v[184:185], v[64:65]
	v_mov_b64_e32 v[182:183], v[62:63]
	v_div_fixup_f32 v169, v171, v169, 1.0
	v_cvt_f32_i32_e32 v185, v185
	v_cvt_f32_i32_e32 v184, v184
	v_cvt_f32_i32_e32 v183, v183
	v_cvt_f32_i32_e32 v182, v182
	v_cvt_f32_i32_e32 v193, v211
	v_cvt_f32_i32_e32 v192, v210
	v_cvt_f32_i32_e32 v211, v213
	v_cvt_f32_i32_e32 v210, v212
	v_mul_f32_e32 v186, v180, v169
	v_pk_mul_f32 v[182:183], v[186:187], v[182:183] op_sel_hi:[0,1]
	v_pk_mul_f32 v[184:185], v[186:187], v[184:185] op_sel_hi:[0,1]
	v_pk_mul_f32 v[210:211], v[186:187], v[210:211] op_sel_hi:[0,1]
	v_pk_mul_f32 v[186:187], v[186:187], v[192:193] op_sel_hi:[0,1]
	v_pk_mul_f32 v[186:187], v[122:123], v[186:187]
	v_pk_mul_f32 v[192:193], v[124:125], v[210:211]
	v_pk_mul_f32 v[184:185], v[128:129], v[184:185]
	v_pk_mul_f32 v[182:183], v[126:127], v[182:183]
	v_pk_mul_f32 v[210:211], v[152:153], v[192:193]
	v_pk_mul_f32 v[212:213], v[150:151], v[186:187]
	v_pk_fma_f32 v[210:211], v[148:149], v[184:185], v[210:211] neg_lo:[0,0,1] neg_hi:[0,0,1]
	v_pk_fma_f32 v[212:213], v[146:147], v[182:183], v[212:213] neg_lo:[0,0,1] neg_hi:[0,0,1]
	v_pk_mul_f32 v[184:185], v[152:153], v[184:185]
	v_pk_mul_f32 v[182:183], v[150:151], v[182:183]
	v_pk_fma_f32 v[184:185], v[148:149], v[192:193], v[184:185]
	v_pk_fma_f32 v[182:183], v[146:147], v[186:187], v[182:183]
	v_mad_i64_i32 v[186:187], s[0:1], v167, s64, v[176:177]
	v_pk_add_f32 v[136:137], v[136:137], v[210:211]
	v_pk_add_f32 v[134:135], v[134:135], v[212:213]
	v_pk_add_f32 v[132:133], v[132:133], v[184:185]
	v_pk_add_f32 v[130:131], v[130:131], v[182:183]
	v_lshl_add_u64 v[186:187], v[186:187], 0, s[2:3]
	v_lshl_add_u64 v[186:187], v[186:187], 0, v[178:179]
	v_cvt_pk_bf16_f32 v192, v212, v213
	v_cvt_pk_bf16_f32 v193, v210, v211
	v_cvt_pk_bf16_f32 v182, v182, v183
	v_cvt_pk_bf16_f32 v183, v184, v185
	global_store_dwordx2 v[186:187], v[192:193], off
	global_store_dwordx2 v[186:187], v[182:183], off offset:128
	ds_read_b128 v[182:185], v157 offset:16
	v_mov_b64_e32 v[212:213], v[56:57]
	v_mov_b64_e32 v[210:211], v[54:55]
	s_waitcnt lgkmcnt(0)
	v_mov_b32_e32 v192, v183
	v_mov_b32_e32 v193, v184
	v_mov_b32_e32 v183, v185
	v_pk_add_f32 v[182:183], v[192:193], v[182:183]
	s_nop 0
	v_add_f32_e32 v157, v182, v183
	v_fmamk_f32 v157, v157, 0x3c000000, v230
	v_cmp_gt_f32_e32 vcc, s63, v157
	v_mul_f32_e32 v167, 0x4f800000, v157
	v_mov_b64_e32 v[184:185], v[52:53]
	v_cndmask_b32_e32 v157, v157, v167, vcc
	v_sqrt_f32_e32 v167, v157
	v_mov_b64_e32 v[182:183], v[50:51]
	v_add_u32_e32 v169, -1, v167
	v_fma_f32 v171, -v169, v167, v157
	v_cmp_ge_f32_e64 s[0:1], 0, v171
	v_add_u32_e32 v171, 1, v167
	v_cvt_f32_i32_e32 v193, v213
	v_cndmask_b32_e64 v169, v167, v169, s[0:1]
	v_fma_f32 v167, -v171, v167, v157
	v_cmp_lt_f32_e64 s[0:1], 0, v167
	v_cvt_f32_i32_e32 v192, v212
	v_cvt_f32_i32_e32 v211, v211
	v_cndmask_b32_e64 v167, v169, v171, s[0:1]
	v_mul_f32_e32 v169, 0x37800000, v167
	v_cndmask_b32_e32 v167, v167, v169, vcc
	v_cmp_class_f32_e32 vcc, v157, v231
	v_cvt_f32_i32_e32 v210, v210
	v_cvt_f32_i32_e32 v183, v183
	v_cndmask_b32_e32 v157, v167, v157, vcc
	v_div_scale_f32 v167, s[0:1], v157, v157, 1.0
	v_rcp_f32_e32 v169, v167
	v_cvt_f32_i32_e32 v182, v182
	v_cvt_f32_i32_e32 v185, v185
	v_cvt_f32_i32_e32 v184, v184
	v_fma_f32 v171, -v167, v169, 1.0
	v_fmac_f32_e32 v169, v171, v169
	v_div_scale_f32 v171, vcc, 1.0, v157, 1.0
	v_mul_f32_e32 v175, v171, v169
	v_fma_f32 v181, -v167, v175, v171
	v_fmac_f32_e32 v175, v181, v169
	v_fma_f32 v167, -v167, v175, v171
	v_div_fmas_f32 v167, v167, v169, v175
	v_div_fixup_f32 v157, v167, v157, 1.0
	v_mul_f32_e32 v180, v180, v157
	v_pk_mul_f32 v[210:211], v[180:181], v[210:211] op_sel_hi:[0,1]
	v_pk_mul_f32 v[192:193], v[180:181], v[192:193] op_sel_hi:[0,1]
	v_pk_mul_f32 v[184:185], v[180:181], v[184:185] op_sel_hi:[0,1]
	v_pk_mul_f32 v[180:181], v[180:181], v[182:183] op_sel_hi:[0,1]
	v_pk_mul_f32 v[192:193], v[128:129], v[192:193]
	v_pk_mul_f32 v[210:211], v[126:127], v[210:211]
	v_pk_mul_f32 v[180:181], v[122:123], v[180:181]
	v_pk_mul_f32 v[182:183], v[124:125], v[184:185]
	v_pk_mul_f32 v[212:213], v[150:151], v[180:181]
	v_pk_mul_f32 v[184:185], v[152:153], v[182:183]
	v_pk_mul_f32 v[152:153], v[152:153], v[192:193]
	v_pk_mul_f32 v[150:151], v[150:151], v[210:211]
	v_pk_fma_f32 v[212:213], v[146:147], v[210:211], v[212:213] neg_lo:[0,0,1] neg_hi:[0,0,1]
	v_pk_fma_f32 v[184:185], v[148:149], v[192:193], v[184:185] neg_lo:[0,0,1] neg_hi:[0,0,1]
	v_pk_fma_f32 v[146:147], v[146:147], v[180:181], v[150:151]
	v_pk_fma_f32 v[148:149], v[148:149], v[182:183], v[152:153]
	v_pk_add_f32 v[144:145], v[144:145], v[184:185]
	v_pk_add_f32 v[142:143], v[142:143], v[212:213]
	v_pk_add_f32 v[140:141], v[140:141], v[148:149]
	v_pk_add_f32 v[138:139], v[138:139], v[146:147]
	v_add_u32_e32 v157, 0x90, v190
	v_cvt_pk_bf16_f32 v150, v212, v213
	v_cvt_pk_bf16_f32 v151, v184, v185
	v_cvt_pk_bf16_f32 v146, v146, v147
	v_add_u32_e32 v167, s19, v157
	v_cvt_pk_bf16_f32 v147, v148, v149
	global_store_dwordx2 v[186:187], v[150:151], off offset:256
	global_store_dwordx2 v[186:187], v[146:147], off offset:384
	v_lshlrev_b32_e32 v146, 8, v167
	v_and_b32_e32 v202, 0x7ff00, v146
	v_lshl_add_u64 v[146:147], s[8:9], 0, v[202:203]
	v_lshl_add_u64 v[150:151], s[16:17], 0, v[202:203]
	v_lshl_add_u64 v[146:147], v[146:147], 0, v[172:173]
	v_lshl_add_u64 v[150:151], v[150:151], 0, v[172:173]
	s_waitcnt vmcnt(4)
	v_mov_b32_e32 v148, v246
	v_mov_b32_e32 v149, v247
	v_lshl_add_u64 v[246:247], v[146:147], 0, s[98:99]
	v_mov_b32_e32 v146, v244
	v_mov_b32_e32 v147, v245
	global_load_dwordx4 v[244:247], v[246:247], off
	v_lshl_add_u32 v157, v157, 5, s21
	v_mov_b32_e32 v152, v252
	v_mov_b32_e32 v153, v253
	v_lshl_add_u64 v[252:253], v[150:151], 0, s[98:99]
	v_mov_b32_e32 v150, v250
	v_mov_b32_e32 v151, v251
	global_load_dwordx4 v[250:253], v[252:253], off
	ds_read_b128 v[180:183], v157
	s_waitcnt lgkmcnt(0)
	v_mov_b32_e32 v184, v181
	v_mov_b32_e32 v185, v182
	v_mov_b32_e32 v181, v183
	v_pk_add_f32 v[180:181], v[184:185], v[180:181]
	v_mov_b64_e32 v[186:187], v[48:49]
	v_add_f32_e32 v169, v180, v181
	v_fmamk_f32 v169, v169, 0x3c000000, v230
	v_cmp_gt_f32_e32 vcc, s63, v169
	v_mul_f32_e32 v171, 0x4f800000, v169
	v_mov_b64_e32 v[184:185], v[46:47]
	v_cndmask_b32_e32 v169, v169, v171, vcc
	v_sqrt_f32_e32 v171, v169
	s_nop 0
	v_add_u32_e32 v175, -1, v171
	v_fma_f32 v180, -v175, v171, v169
	v_cmp_ge_f32_e64 s[0:1], 0, v180
	v_add_u32_e32 v180, 1, v171
	s_nop 0
	v_cndmask_b32_e64 v175, v171, v175, s[0:1]
	v_fma_f32 v171, -v180, v171, v169
	v_cmp_lt_f32_e64 s[0:1], 0, v171
	s_nop 1
	v_cndmask_b32_e64 v171, v175, v180, s[0:1]
	v_mul_f32_e32 v175, 0x37800000, v171
	v_cndmask_b32_e32 v171, v171, v175, vcc
	v_cmp_class_f32_e32 vcc, v169, v231
	s_nop 1
	v_cndmask_b32_e32 v169, v171, v169, vcc
	v_div_scale_f32 v171, s[0:1], v169, v169, 1.0
	v_rcp_f32_e32 v175, v171
	s_nop 0
	v_fma_f32 v180, -v171, v175, 1.0
	v_fmac_f32_e32 v175, v180, v175
	v_div_scale_f32 v180, vcc, 1.0, v169, 1.0
	v_mul_f32_e32 v181, v180, v175
	v_fma_f32 v182, -v171, v181, v180
	v_fmac_f32_e32 v181, v182, v175
	v_fma_f32 v171, -v171, v181, v180
	v_div_fmas_f32 v171, v171, v175, v181
	v_mov_b64_e32 v[182:183], v[44:45]
	v_mov_b64_e32 v[180:181], v[42:43]
	v_div_fixup_f32 v169, v171, v169, 1.0
	v_cvt_f32_i32_e32 v181, v181
	v_cvt_f32_i32_e32 v180, v180
	v_cvt_f32_i32_e32 v183, v183
	v_cvt_f32_i32_e32 v182, v182
	v_cvt_f32_i32_e32 v187, v187
	v_cvt_f32_i32_e32 v186, v186
	v_cvt_f32_i32_e32 v185, v185
	v_cvt_f32_i32_e32 v184, v184
	v_mul_f32_e32 v192, v174, v169
	v_pk_mul_f32 v[182:183], v[192:193], v[182:183] op_sel_hi:[0,1]
	v_pk_mul_f32 v[180:181], v[192:193], v[180:181] op_sel_hi:[0,1]
	v_pk_mul_f32 v[184:185], v[192:193], v[184:185] op_sel_hi:[0,1]
	v_pk_mul_f32 v[186:187], v[192:193], v[186:187] op_sel_hi:[0,1]
	v_pk_mul_f32 v[180:181], v[122:123], v[180:181]
	v_pk_mul_f32 v[182:183], v[124:125], v[182:183]
	v_pk_mul_f32 v[186:187], v[128:129], v[186:187]
	v_pk_mul_f32 v[184:185], v[126:127], v[184:185]
	v_pk_mul_f32 v[192:193], v[152:153], v[182:183]
	v_pk_mul_f32 v[210:211], v[150:151], v[180:181]
	v_pk_fma_f32 v[192:193], v[148:149], v[186:187], v[192:193] neg_lo:[0,0,1] neg_hi:[0,0,1]
	v_pk_fma_f32 v[210:211], v[146:147], v[184:185], v[210:211] neg_lo:[0,0,1] neg_hi:[0,0,1]
	v_pk_mul_f32 v[186:187], v[152:153], v[186:187]
	v_pk_mul_f32 v[184:185], v[150:151], v[184:185]
	v_pk_fma_f32 v[182:183], v[148:149], v[182:183], v[186:187]
	v_pk_fma_f32 v[180:181], v[146:147], v[180:181], v[184:185]
	v_mad_i64_i32 v[184:185], s[0:1], v167, s64, v[176:177]
	v_pk_add_f32 v[136:137], v[136:137], v[192:193]
	v_pk_add_f32 v[134:135], v[134:135], v[210:211]
	v_pk_add_f32 v[132:133], v[132:133], v[182:183]
	v_pk_add_f32 v[130:131], v[130:131], v[180:181]
	v_lshl_add_u64 v[184:185], v[184:185], 0, s[2:3]
	v_lshl_add_u64 v[212:213], v[184:185], 0, v[178:179]
	v_cvt_pk_bf16_f32 v184, v210, v211
	v_cvt_pk_bf16_f32 v185, v192, v193
	v_cvt_pk_bf16_f32 v180, v180, v181
	v_cvt_pk_bf16_f32 v181, v182, v183
	global_store_dwordx2 v[212:213], v[184:185], off
	global_store_dwordx2 v[212:213], v[180:181], off offset:128
	ds_read_b128 v[180:183], v157 offset:16
	s_waitcnt lgkmcnt(0)
	v_mov_b32_e32 v184, v181
	v_mov_b32_e32 v185, v182
	v_mov_b32_e32 v181, v183
	v_pk_add_f32 v[180:181], v[184:185], v[180:181]
	v_mov_b64_e32 v[186:187], v[36:37]
	v_add_f32_e32 v157, v180, v181
	v_fmamk_f32 v157, v157, 0x3c000000, v230
	v_cmp_gt_f32_e32 vcc, s63, v157
	v_mul_f32_e32 v167, 0x4f800000, v157
	v_mov_b64_e32 v[184:185], v[34:35]
	v_cndmask_b32_e32 v157, v157, v167, vcc
	v_sqrt_f32_e32 v167, v157
	s_nop 0
	v_add_u32_e32 v169, -1, v167
	v_fma_f32 v171, -v169, v167, v157
	v_cmp_ge_f32_e64 s[0:1], 0, v171
	v_add_u32_e32 v171, 1, v167
	s_nop 0
	v_cndmask_b32_e64 v169, v167, v169, s[0:1]
	v_fma_f32 v167, -v171, v167, v157
	v_cmp_lt_f32_e64 s[0:1], 0, v167
	s_nop 1
	v_cndmask_b32_e64 v167, v169, v171, s[0:1]
	v_mul_f32_e32 v169, 0x37800000, v167
	v_cndmask_b32_e32 v167, v167, v169, vcc
	v_cmp_class_f32_e32 vcc, v157, v231
	s_nop 1
	v_cndmask_b32_e32 v157, v167, v157, vcc
	v_div_scale_f32 v167, s[0:1], v157, v157, 1.0
	v_rcp_f32_e32 v169, v167
	s_nop 0
	v_fma_f32 v171, -v167, v169, 1.0
	v_fmac_f32_e32 v169, v171, v169
	v_div_scale_f32 v171, vcc, 1.0, v157, 1.0
	v_mul_f32_e32 v175, v171, v169
	v_fma_f32 v180, -v167, v175, v171
	v_fmac_f32_e32 v175, v180, v169
	v_mov_b64_e32 v[182:183], v[40:41]
	v_mov_b64_e32 v[180:181], v[38:39]
	v_fma_f32 v167, -v167, v175, v171
	v_cvt_f32_i32_e32 v183, v183
	v_cvt_f32_i32_e32 v182, v182
	v_cvt_f32_i32_e32 v181, v181
	v_cvt_f32_i32_e32 v180, v180
	v_cvt_f32_i32_e32 v185, v185
	v_cvt_f32_i32_e32 v184, v184
	v_cvt_f32_i32_e32 v187, v187
	v_cvt_f32_i32_e32 v186, v186
	v_div_fmas_f32 v167, v167, v169, v175
	v_div_fixup_f32 v157, v167, v157, 1.0
	v_mul_f32_e32 v174, v174, v157
	v_pk_mul_f32 v[180:181], v[174:175], v[180:181] op_sel_hi:[0,1]
	v_pk_mul_f32 v[182:183], v[174:175], v[182:183] op_sel_hi:[0,1]
	v_pk_mul_f32 v[186:187], v[174:175], v[186:187] op_sel_hi:[0,1]
	v_pk_mul_f32 v[174:175], v[174:175], v[184:185] op_sel_hi:[0,1]
	v_pk_mul_f32 v[182:183], v[128:129], v[182:183]
	v_pk_mul_f32 v[180:181], v[126:127], v[180:181]
	v_pk_mul_f32 v[174:175], v[122:123], v[174:175]
	v_pk_mul_f32 v[184:185], v[124:125], v[186:187]
	v_pk_mul_f32 v[192:193], v[150:151], v[174:175]
	v_pk_mul_f32 v[186:187], v[152:153], v[184:185]
	v_pk_mul_f32 v[152:153], v[152:153], v[182:183]
	v_pk_mul_f32 v[150:151], v[150:151], v[180:181]
	v_pk_fma_f32 v[192:193], v[146:147], v[180:181], v[192:193] neg_lo:[0,0,1] neg_hi:[0,0,1]
	v_pk_fma_f32 v[186:187], v[148:149], v[182:183], v[186:187] neg_lo:[0,0,1] neg_hi:[0,0,1]
	v_pk_fma_f32 v[150:151], v[146:147], v[174:175], v[150:151]
	v_pk_fma_f32 v[152:153], v[148:149], v[184:185], v[152:153]
	v_pk_add_f32 v[144:145], v[144:145], v[186:187]
	v_pk_add_f32 v[142:143], v[142:143], v[192:193]
	v_pk_add_f32 v[148:149], v[140:141], v[152:153]
	v_pk_add_f32 v[146:147], v[138:139], v[150:151]
	v_add_u32_e32 v157, 0xa0, v190
	v_cvt_pk_bf16_f32 v138, v192, v193
	v_cvt_pk_bf16_f32 v139, v186, v187
	v_add_u32_e32 v167, s19, v157
	v_cvt_pk_bf16_f32 v140, v150, v151
	v_cvt_pk_bf16_f32 v141, v152, v153
	global_store_dwordx2 v[212:213], v[138:139], off offset:256
	global_store_dwordx2 v[212:213], v[140:141], off offset:384
	v_lshlrev_b32_e32 v138, 8, v167
	v_and_b32_e32 v202, 0x7ff00, v138
	v_lshl_add_u64 v[138:139], s[8:9], 0, v[202:203]
	v_lshl_add_u64 v[150:151], s[16:17], 0, v[202:203]
	v_lshl_add_u64 v[138:139], v[138:139], 0, v[172:173]
	v_lshl_add_u64 v[150:151], v[150:151], 0, v[172:173]
	s_waitcnt vmcnt(4)
	v_mov_b32_e32 v140, v246
	v_mov_b32_e32 v141, v247
	v_lshl_add_u64 v[246:247], v[138:139], 0, s[98:99]
	v_mov_b32_e32 v138, v244
	v_mov_b32_e32 v139, v245
	global_load_dwordx4 v[244:247], v[246:247], off
	v_lshl_add_u32 v157, v157, 5, s21
	v_mov_b32_e32 v152, v252
	v_mov_b32_e32 v153, v253
	v_lshl_add_u64 v[252:253], v[150:151], 0, s[98:99]
	v_mov_b32_e32 v150, v250
	v_mov_b32_e32 v151, v251
	global_load_dwordx4 v[250:253], v[252:253], off
	ds_read_b128 v[180:183], v157
	v_mov_b64_e32 v[186:187], v[32:33]
	v_mov_b64_e32 v[184:185], v[30:31]
	s_waitcnt lgkmcnt(0)
	v_mov_b32_e32 v174, v181
	v_mov_b32_e32 v175, v182
	v_mov_b32_e32 v181, v183
	v_pk_add_f32 v[174:175], v[174:175], v[180:181]
	s_nop 0
	v_add_f32_e32 v169, v174, v175
	v_fmamk_f32 v169, v169, 0x3c000000, v230
	v_cmp_gt_f32_e32 vcc, s63, v169
	v_mul_f32_e32 v171, 0x4f800000, v169
	s_nop 0
	v_cndmask_b32_e32 v169, v169, v171, vcc
	v_sqrt_f32_e32 v171, v169
	s_nop 0
	v_add_u32_e32 v174, -1, v171
	v_fma_f32 v175, -v174, v171, v169
	v_cmp_ge_f32_e64 s[0:1], 0, v175
	v_add_u32_e32 v175, 1, v171
	s_nop 0
	v_cndmask_b32_e64 v174, v171, v174, s[0:1]
	v_fma_f32 v171, -v175, v171, v169
	v_cmp_lt_f32_e64 s[0:1], 0, v171
	s_nop 1
	v_cndmask_b32_e64 v171, v174, v175, s[0:1]
	v_mul_f32_e32 v174, 0x37800000, v171
	v_cndmask_b32_e32 v171, v171, v174, vcc
	v_cmp_class_f32_e32 vcc, v169, v231
	s_nop 1
	v_cndmask_b32_e32 v169, v171, v169, vcc
	v_div_scale_f32 v171, s[0:1], v169, v169, 1.0
	v_rcp_f32_e32 v174, v171
	s_nop 0
	v_fma_f32 v175, -v171, v174, 1.0
	v_fmac_f32_e32 v174, v175, v174
	v_div_scale_f32 v175, vcc, 1.0, v169, 1.0
	v_mul_f32_e32 v180, v175, v174
	v_fma_f32 v181, -v171, v180, v175
	v_fmac_f32_e32 v180, v181, v174
	v_fma_f32 v171, -v171, v180, v175
	v_div_fmas_f32 v171, v171, v174, v180
	v_mov_b64_e32 v[182:183], v[28:29]
	v_mov_b64_e32 v[180:181], v[26:27]
	v_div_fixup_f32 v169, v171, v169, 1.0
	v_cvt_f32_i32_e32 v181, v181
	v_cvt_f32_i32_e32 v180, v180
	v_cvt_f32_i32_e32 v183, v183
	v_cvt_f32_i32_e32 v182, v182
	v_cvt_f32_i32_e32 v175, v187
	v_cvt_f32_i32_e32 v174, v186
	v_cvt_f32_i32_e32 v185, v185
	v_cvt_f32_i32_e32 v184, v184
	v_mul_f32_e32 v186, v170, v169
	v_pk_mul_f32 v[182:183], v[186:187], v[182:183] op_sel_hi:[0,1]
	v_pk_mul_f32 v[180:181], v[186:187], v[180:181] op_sel_hi:[0,1]
	v_pk_mul_f32 v[184:185], v[186:187], v[184:185] op_sel_hi:[0,1]
	v_pk_mul_f32 v[174:175], v[186:187], v[174:175] op_sel_hi:[0,1]
	v_pk_mul_f32 v[180:181], v[122:123], v[180:181]
	v_pk_mul_f32 v[182:183], v[124:125], v[182:183]
	v_pk_mul_f32 v[174:175], v[128:129], v[174:175]
	v_pk_mul_f32 v[184:185], v[126:127], v[184:185]
	v_pk_mul_f32 v[186:187], v[152:153], v[182:183]
	v_pk_mul_f32 v[192:193], v[150:151], v[180:181]
	v_pk_fma_f32 v[186:187], v[140:141], v[174:175], v[186:187] neg_lo:[0,0,1] neg_hi:[0,0,1]
	v_pk_fma_f32 v[192:193], v[138:139], v[184:185], v[192:193] neg_lo:[0,0,1] neg_hi:[0,0,1]
	v_pk_mul_f32 v[174:175], v[152:153], v[174:175]
	v_pk_mul_f32 v[184:185], v[150:151], v[184:185]
	v_pk_fma_f32 v[174:175], v[140:141], v[182:183], v[174:175]
	v_pk_fma_f32 v[180:181], v[138:139], v[180:181], v[184:185]
	v_mad_i64_i32 v[182:183], s[0:1], v167, s64, v[176:177]
	v_pk_add_f32 v[136:137], v[136:137], v[186:187]
	v_pk_add_f32 v[134:135], v[134:135], v[192:193]
	v_pk_add_f32 v[132:133], v[132:133], v[174:175]
	v_pk_add_f32 v[130:131], v[130:131], v[180:181]
	v_lshl_add_u64 v[182:183], v[182:183], 0, s[2:3]
	v_lshl_add_u64 v[210:211], v[182:183], 0, v[178:179]
	v_cvt_pk_bf16_f32 v182, v192, v193
	v_cvt_pk_bf16_f32 v183, v186, v187
	v_cvt_pk_bf16_f32 v180, v180, v181
	v_cvt_pk_bf16_f32 v181, v174, v175
	global_store_dwordx2 v[210:211], v[182:183], off
	global_store_dwordx2 v[210:211], v[180:181], off offset:128
	ds_read_b128 v[180:183], v157 offset:16
	v_mov_b64_e32 v[186:187], v[20:21]
	v_mov_b64_e32 v[184:185], v[18:19]
	s_waitcnt lgkmcnt(0)
	v_mov_b32_e32 v174, v181
	v_mov_b32_e32 v175, v182
	v_mov_b32_e32 v181, v183
	v_pk_add_f32 v[174:175], v[174:175], v[180:181]
	v_mov_b64_e32 v[182:183], v[24:25]
	v_add_f32_e32 v157, v174, v175
	v_fmamk_f32 v157, v157, 0x3c000000, v230
	v_cmp_gt_f32_e32 vcc, s63, v157
	v_mul_f32_e32 v167, 0x4f800000, v157
	v_mov_b64_e32 v[180:181], v[22:23]
	v_cndmask_b32_e32 v157, v157, v167, vcc
	v_sqrt_f32_e32 v167, v157
	s_nop 0
	v_cvt_f32_i32_e32 v181, v181
	v_add_u32_e32 v169, -1, v167
	v_fma_f32 v171, -v169, v167, v157
	v_cmp_ge_f32_e64 s[0:1], 0, v171
	v_add_u32_e32 v171, 1, v167
	v_cvt_f32_i32_e32 v180, v180
	v_cndmask_b32_e64 v169, v167, v169, s[0:1]
	v_fma_f32 v167, -v171, v167, v157
	v_cmp_lt_f32_e64 s[0:1], 0, v167
	s_nop 1
	v_cndmask_b32_e64 v167, v169, v171, s[0:1]
	v_mul_f32_e32 v169, 0x37800000, v167
	v_cndmask_b32_e32 v167, v167, v169, vcc
	v_cmp_class_f32_e32 vcc, v157, v231
	s_nop 1
	v_cndmask_b32_e32 v157, v167, v157, vcc
	v_div_scale_f32 v167, s[0:1], v157, v157, 1.0
	v_rcp_f32_e32 v169, v167
	s_nop 0
	v_fma_f32 v171, -v167, v169, 1.0
	v_fmac_f32_e32 v169, v171, v169
	v_div_scale_f32 v171, vcc, 1.0, v157, 1.0
	v_mul_f32_e32 v174, v171, v169
	v_fma_f32 v175, -v167, v174, v171
	v_fmac_f32_e32 v174, v175, v169
	v_fma_f32 v167, -v167, v174, v171
	v_div_fmas_f32 v167, v167, v169, v174
	v_cvt_f32_i32_e32 v175, v183
	v_cvt_f32_i32_e32 v174, v182
	v_cvt_f32_i32_e32 v183, v185
	v_cvt_f32_i32_e32 v182, v184
	v_cvt_f32_i32_e32 v185, v187
	v_cvt_f32_i32_e32 v184, v186
	v_div_fixup_f32 v157, v167, v157, 1.0
	v_mul_f32_e32 v170, v170, v157
	v_pk_mul_f32 v[180:181], v[170:171], v[180:181] op_sel_hi:[0,1]
	v_pk_mul_f32 v[174:175], v[170:171], v[174:175] op_sel_hi:[0,1]
	v_pk_mul_f32 v[184:185], v[170:171], v[184:185] op_sel_hi:[0,1]
	v_pk_mul_f32 v[170:171], v[170:171], v[182:183] op_sel_hi:[0,1]
	v_pk_mul_f32 v[174:175], v[128:129], v[174:175]
	v_pk_mul_f32 v[180:181], v[126:127], v[180:181]
	v_pk_mul_f32 v[170:171], v[122:123], v[170:171]
	v_pk_mul_f32 v[182:183], v[124:125], v[184:185]
	v_pk_mul_f32 v[186:187], v[150:151], v[170:171]
	v_pk_mul_f32 v[184:185], v[152:153], v[182:183]
	v_pk_mul_f32 v[152:153], v[152:153], v[174:175]
	v_pk_mul_f32 v[150:151], v[150:151], v[180:181]
	v_pk_fma_f32 v[186:187], v[138:139], v[180:181], v[186:187] neg_lo:[0,0,1] neg_hi:[0,0,1]
	v_pk_fma_f32 v[184:185], v[140:141], v[174:175], v[184:185] neg_lo:[0,0,1] neg_hi:[0,0,1]
	v_pk_fma_f32 v[150:151], v[138:139], v[170:171], v[150:151]
	v_pk_fma_f32 v[152:153], v[140:141], v[182:183], v[152:153]
	v_pk_add_f32 v[140:141], v[144:145], v[184:185]
	v_pk_add_f32 v[138:139], v[142:143], v[186:187]
	v_pk_add_f32 v[144:145], v[148:149], v[152:153]
	v_pk_add_f32 v[142:143], v[146:147], v[150:151]
	v_add_u32_e32 v157, 0xb0, v190
	v_cvt_pk_bf16_f32 v146, v186, v187
	v_cvt_pk_bf16_f32 v147, v184, v185
	v_add_u32_e32 v167, s19, v157
	v_cvt_pk_bf16_f32 v148, v150, v151
	v_cvt_pk_bf16_f32 v149, v152, v153
	global_store_dwordx2 v[210:211], v[146:147], off offset:256
	global_store_dwordx2 v[210:211], v[148:149], off offset:384
	v_lshlrev_b32_e32 v146, 8, v167
	v_and_b32_e32 v202, 0x7ff00, v146
	v_lshl_add_u64 v[146:147], s[8:9], 0, v[202:203]
	v_lshl_add_u64 v[150:151], s[16:17], 0, v[202:203]
	v_lshl_add_u64 v[146:147], v[146:147], 0, v[172:173]
	v_lshl_add_u64 v[150:151], v[150:151], 0, v[172:173]
	s_waitcnt vmcnt(4)
	v_mov_b32_e32 v146, v244
	v_mov_b32_e32 v147, v245
	v_mov_b32_e32 v148, v246
	v_mov_b32_e32 v149, v247
	v_lshl_add_u32 v157, v157, 5, s21
	v_mov_b32_e32 v150, v250
	v_mov_b32_e32 v151, v251
	v_mov_b32_e32 v152, v252
	v_mov_b32_e32 v153, v253
	ds_read_b128 v[170:173], v157
	v_mov_b64_e32 v[182:183], v[16:17]
	v_mov_b64_e32 v[180:181], v[14:15]
	s_waitcnt lgkmcnt(0)
	v_mov_b32_e32 v174, v171
	v_mov_b32_e32 v175, v172
	v_mov_b32_e32 v171, v173
	v_pk_add_f32 v[170:171], v[174:175], v[170:171]
	s_nop 0
	v_add_f32_e32 v169, v170, v171
	v_fmamk_f32 v169, v169, 0x3c000000, v230
	v_cmp_gt_f32_e32 vcc, s63, v169
	v_mul_f32_e32 v170, 0x4f800000, v169
	s_nop 0
	v_cndmask_b32_e32 v169, v169, v170, vcc
	v_sqrt_f32_e32 v170, v169
	s_nop 0
	v_add_u32_e32 v171, -1, v170
	v_fma_f32 v172, -v171, v170, v169
	v_cmp_ge_f32_e64 s[0:1], 0, v172
	v_add_u32_e32 v172, 1, v170
	s_nop 0
	v_cndmask_b32_e64 v171, v170, v171, s[0:1]
	v_fma_f32 v170, -v172, v170, v169
	v_cmp_lt_f32_e64 s[0:1], 0, v170
	s_nop 1
	v_cndmask_b32_e64 v170, v171, v172, s[0:1]
	v_mul_f32_e32 v171, 0x37800000, v170
	v_cndmask_b32_e32 v170, v170, v171, vcc
	v_cmp_class_f32_e32 vcc, v169, v231
	s_nop 1
	v_cndmask_b32_e32 v169, v170, v169, vcc
	v_div_scale_f32 v170, s[0:1], v169, v169, 1.0
	v_rcp_f32_e32 v171, v170
	s_nop 0
	v_fma_f32 v172, -v170, v171, 1.0
	v_fmac_f32_e32 v171, v172, v171
	v_div_scale_f32 v172, vcc, 1.0, v169, 1.0
	v_mul_f32_e32 v173, v172, v171
	v_fma_f32 v174, -v170, v173, v172
	v_fmac_f32_e32 v173, v174, v171
	v_fma_f32 v170, -v170, v173, v172
	v_div_fmas_f32 v170, v170, v171, v173
	v_div_fixup_f32 v169, v170, v169, 1.0
	v_mov_b64_e32 v[172:173], v[12:13]
	v_mov_b64_e32 v[170:171], v[10:11]
	s_nop 0
	v_cvt_f32_i32_e32 v171, v171
	v_cvt_f32_i32_e32 v170, v170
	v_cvt_f32_i32_e32 v173, v173
	v_cvt_f32_i32_e32 v172, v172
	v_cvt_f32_i32_e32 v175, v183
	v_cvt_f32_i32_e32 v174, v182
	v_cvt_f32_i32_e32 v181, v181
	v_cvt_f32_i32_e32 v180, v180
	v_mul_f32_e32 v182, v166, v169
	v_pk_mul_f32 v[172:173], v[182:183], v[172:173] op_sel_hi:[0,1]
	v_pk_mul_f32 v[170:171], v[182:183], v[170:171] op_sel_hi:[0,1]
	v_pk_mul_f32 v[180:181], v[182:183], v[180:181] op_sel_hi:[0,1]
	v_pk_mul_f32 v[174:175], v[182:183], v[174:175] op_sel_hi:[0,1]
	v_pk_mul_f32 v[170:171], v[122:123], v[170:171]
	v_pk_mul_f32 v[172:173], v[124:125], v[172:173]
	v_pk_mul_f32 v[174:175], v[128:129], v[174:175]
	v_pk_mul_f32 v[180:181], v[126:127], v[180:181]
	v_pk_mul_f32 v[182:183], v[152:153], v[172:173]
	v_pk_mul_f32 v[184:185], v[150:151], v[170:171]
	v_pk_fma_f32 v[182:183], v[148:149], v[174:175], v[182:183] neg_lo:[0,0,1] neg_hi:[0,0,1]
	v_pk_fma_f32 v[184:185], v[146:147], v[180:181], v[184:185] neg_lo:[0,0,1] neg_hi:[0,0,1]
	v_pk_mul_f32 v[174:175], v[152:153], v[174:175]
	v_pk_mul_f32 v[180:181], v[150:151], v[180:181]
	v_pk_fma_f32 v[172:173], v[148:149], v[172:173], v[174:175]
	v_pk_fma_f32 v[170:171], v[146:147], v[170:171], v[180:181]
	v_mad_i64_i32 v[174:175], s[0:1], v167, s64, v[176:177]
	v_pk_add_f32 v[136:137], v[136:137], v[182:183]
	v_pk_add_f32 v[134:135], v[134:135], v[184:185]
	v_pk_add_f32 v[132:133], v[132:133], v[172:173]
	v_pk_add_f32 v[130:131], v[130:131], v[170:171]
	v_lshl_add_u64 v[174:175], v[174:175], 0, s[2:3]
	v_lshl_add_u64 v[178:179], v[174:175], 0, v[178:179]
	v_cvt_pk_bf16_f32 v174, v184, v185
	v_cvt_pk_bf16_f32 v175, v182, v183
	v_cvt_pk_bf16_f32 v170, v170, v171
	v_cvt_pk_bf16_f32 v171, v172, v173
	global_store_dwordx2 v[178:179], v[174:175], off
	global_store_dwordx2 v[178:179], v[170:171], off offset:128
	ds_read_b128 v[170:173], v157 offset:16
	s_waitcnt lgkmcnt(0)
	v_mov_b32_e32 v174, v171
	v_mov_b32_e32 v175, v172
	v_mov_b32_e32 v171, v173
	v_pk_add_f32 v[170:171], v[174:175], v[170:171]
	v_mov_b64_e32 v[176:177], v[4:5]
	v_add_f32_e32 v157, v170, v171
	v_fmamk_f32 v157, v157, 0x3c000000, v230
	v_cmp_gt_f32_e32 vcc, s63, v157
	v_mul_f32_e32 v167, 0x4f800000, v157
	v_mov_b64_e32 v[174:175], v[2:3]
	v_cndmask_b32_e32 v157, v157, v167, vcc
	v_sqrt_f32_e32 v167, v157
	s_nop 0
	v_add_u32_e32 v169, -1, v167
	v_fma_f32 v170, -v169, v167, v157
	v_cmp_ge_f32_e64 s[0:1], 0, v170
	v_add_u32_e32 v170, 1, v167
	s_nop 0
	v_cndmask_b32_e64 v169, v167, v169, s[0:1]
	v_fma_f32 v167, -v170, v167, v157
	v_cmp_lt_f32_e64 s[0:1], 0, v167
	s_nop 1
	v_cndmask_b32_e64 v167, v169, v170, s[0:1]
	v_mul_f32_e32 v169, 0x37800000, v167
	v_cndmask_b32_e32 v167, v167, v169, vcc
	v_cmp_class_f32_e32 vcc, v157, v231
	s_nop 1
	v_cndmask_b32_e32 v157, v167, v157, vcc
	v_div_scale_f32 v167, s[0:1], v157, v157, 1.0
	v_rcp_f32_e32 v169, v167
	s_nop 0
	v_fma_f32 v170, -v167, v169, 1.0
	v_fmac_f32_e32 v169, v170, v169
	v_div_scale_f32 v170, vcc, 1.0, v157, 1.0
	v_mul_f32_e32 v171, v170, v169
	v_fma_f32 v172, -v167, v171, v170
	v_fmac_f32_e32 v171, v172, v169
	v_fma_f32 v167, -v167, v171, v170
	v_div_fmas_f32 v167, v167, v169, v171
	v_mov_b64_e32 v[172:173], v[8:9]
	v_mov_b64_e32 v[170:171], v[6:7]
	v_div_fixup_f32 v157, v167, v157, 1.0
	v_cvt_f32_i32_e32 v173, v173
	v_cvt_f32_i32_e32 v172, v172
	v_cvt_f32_i32_e32 v171, v171
	v_cvt_f32_i32_e32 v170, v170
	v_mul_f32_e32 v166, v166, v157
	v_pk_mul_f32 v[172:173], v[166:167], v[172:173] op_sel_hi:[0,1]
	v_pk_mul_f32 v[128:129], v[128:129], v[172:173]
	v_pk_mul_f32 v[170:171], v[166:167], v[170:171] op_sel_hi:[0,1]
	v_pk_mul_f32 v[126:127], v[126:127], v[170:171]
	v_cvt_f32_i32_e32 v171, v175
	v_cvt_f32_i32_e32 v170, v174
	v_cvt_f32_i32_e32 v173, v177
	v_cvt_f32_i32_e32 v172, v176
	v_pk_mul_f32 v[172:173], v[166:167], v[172:173] op_sel_hi:[0,1]
	v_pk_mul_f32 v[166:167], v[166:167], v[170:171] op_sel_hi:[0,1]
	v_pk_mul_f32 v[122:123], v[122:123], v[166:167]
	v_pk_mul_f32 v[124:125], v[124:125], v[172:173]
	v_pk_mul_f32 v[170:171], v[150:151], v[122:123]
	v_pk_mul_f32 v[166:167], v[152:153], v[124:125]
	v_pk_fma_f32 v[170:171], v[146:147], v[126:127], v[170:171] neg_lo:[0,0,1] neg_hi:[0,0,1]
	v_pk_fma_f32 v[166:167], v[148:149], v[128:129], v[166:167] neg_lo:[0,0,1] neg_hi:[0,0,1]
	v_pk_mul_f32 v[128:129], v[152:153], v[128:129]
	v_pk_mul_f32 v[126:127], v[150:151], v[126:127]
	v_pk_fma_f32 v[148:149], v[148:149], v[124:125], v[128:129]
	v_pk_fma_f32 v[146:147], v[146:147], v[122:123], v[126:127]
	v_pk_add_f32 v[128:129], v[140:141], v[166:167]
	v_pk_add_f32 v[126:127], v[138:139], v[170:171]
	v_pk_add_f32 v[124:125], v[144:145], v[148:149]
	v_pk_add_f32 v[122:123], v[142:143], v[146:147]
	s_nop 0
	v_cvt_pk_bf16_f32 v138, v170, v171
	v_cvt_pk_bf16_f32 v139, v166, v167
	v_cvt_pk_bf16_f32 v140, v146, v147
	v_cvt_pk_bf16_f32 v141, v148, v149
	global_store_dwordx2 v[178:179], v[138:139], off offset:256
	global_store_dwordx2 v[178:179], v[140:141], off offset:384
	s_cbranch_scc1 .LBB0_2583
	v_xor_b32_e32 v138, 1, v234
	v_cmp_lt_i32_e32 vcc, v138, v155
	v_xor_b32_e32 v139, 2, v234
	s_nop 0
	v_cndmask_b32_e32 v138, v234, v138, vcc
	v_lshlrev_b32_e32 v138, 2, v138
	ds_bpermute_b32 v143, v138, v134
	v_cmp_lt_i32_e32 vcc, v139, v155
	s_waitcnt lgkmcnt(0)
	v_add_f32_e32 v134, v134, v143
	v_cndmask_b32_e32 v139, v234, v139, vcc
	v_lshlrev_b32_e32 v140, 2, v139
	ds_bpermute_b32 v143, v140, v134
	v_xor_b32_e32 v139, 4, v234
	v_cmp_lt_i32_e32 vcc, v139, v155
	s_waitcnt lgkmcnt(0)
	v_add_f32_e32 v134, v134, v143
	v_cndmask_b32_e32 v139, v234, v139, vcc
	v_lshlrev_b32_e32 v141, 2, v139
	ds_bpermute_b32 v143, v141, v134
	v_xor_b32_e32 v139, 8, v234
	v_cmp_lt_i32_e32 vcc, v139, v155
	s_waitcnt lgkmcnt(0)
	v_add_f32_e32 v134, v134, v143
	v_cndmask_b32_e32 v139, v234, v139, vcc
	v_lshlrev_b32_e32 v142, 2, v139
	ds_bpermute_b32 v143, v142, v134
	v_cmp_eq_u32_e32 vcc, 0, v189
	v_lshl_add_u32 v139, v168, 2, s60
	s_and_saveexec_b64 s[0:1], vcc
	s_cbranch_execz .LBB0_2550
	s_waitcnt lgkmcnt(0)
	v_add_f32_e32 v134, v134, v143
	ds_write_b32 v139, v134
